# E15: E14 + gsz==8 shift/and fast path around the tile_of software division in the G1/G2 unit heads and G1 epilogue next2
# speedup vs baseline: 1.0014x; 1.0014x over previous
.LBB0_1199:
	s_or_b64 exec, exec, s[0:1]
	v_readlane_b32 s0, v252, 2
	v_mov_b32_e32 v0, 0x108000
	v_readlane_b32 s1, v252, 3
	s_waitcnt lgkmcnt(0)
	s_barrier
	s_add_u32 s8, s0, 0x108000
	s_addc_u32 s9, s1, 0
	s_nop 0
	global_load_dword v0, v0, s[0:1]
	s_add_u32 s33, s0, 0x108100
	s_addc_u32 s50, s1, 0
	s_mov_b32 s100, s33
	s_mov_b32 s101, s50
	v_lshlrev_b32_e32 v240, 2, v226
	global_load_dword v241, v240, s[100:101]
	global_load_dword v242, v240, s[100:101] offset:2048
	v_add_u32_e32 v240, 0x21000, v240
	s_waitcnt vmcnt(0)
	ds_write_b32 v240, v241
	ds_write_b32 v240, v242 offset:2048
	s_waitcnt lgkmcnt(0)
	s_barrier
	v_readlane_b32 s0, v252, 0
	v_mov_b32_e32 v6, v226
	v_readlane_b32 s1, v252, 1
	s_waitcnt vmcnt(0)
	v_lshlrev_b32_e32 v162, 4, v0
	v_cmp_ge_i32_e32 vcc, s0, v162
	v_readfirstlane_b32 s31, v0
	v_readfirstlane_b32 s6, v6
	v_cmp_lt_i32_e64 s[0:1], s0, v162
	s_cbranch_vccnz .LBB0_1201
	v_readlane_b32 s2, v252, 0
	s_mov_b32 s4, s2
	s_ashr_i32 s2, s2, 31
	s_lshr_b32 s2, s2, 29
	v_readlane_b32 s3, v252, 1
	s_add_i32 s2, s4, s2
	s_and_b32 s3, s2, -8
	s_sub_i32 s3, s4, s3
	v_mov_b32_e32 v0, s3
	v_alignbit_b32 v0, s31, v0, 31
	s_ashr_i32 s2, s2, 3
	v_readfirstlane_b32 s4, v0
	s_mul_i32 s3, s4, s3
	s_add_i32 s2, s3, s2
	s_ashr_i32 s3, s2, 31
	s_lshr_b32 s3, s3, 25
	s_add_i32 s3, s2, s3
	s_ashr_i32 s4, s3, 7
	s_lshl_b32 s4, s4, 3
	s_sub_i32 s5, s31, s4
	s_min_i32 s5, s5, 8
	s_and_b32 s3, s3, 0xffffff80
	s_sub_i32 s2, s2, s3
	s_cmp_eq_u32 s5, 8
	s_cbranch_scc0 .Ldivslow_1
	s_ashr_i32 s10, s2, 3
	s_and_b32 s2, s2, 7
	s_branch .Ldivjoin_1
.Ldivslow_1:
	s_abs_i32 s7, s5
	v_cvt_f32_u32_e32 v0, s7
	s_sub_i32 s11, 0, s7
	v_rcp_iflag_f32_e32 v0, v0
	s_abs_i32 s3, s2
	s_xor_b32 s10, s2, s5
	s_ashr_i32 s10, s10, 31
	v_mul_f32_e32 v0, 0x4f7ffffe, v0
	v_cvt_u32_f32_e32 v0, v0
	s_nop 0
	v_readfirstlane_b32 s12, v0
	s_mul_i32 s11, s11, s12
	s_mul_hi_u32 s11, s12, s11
	s_add_i32 s12, s12, s11
	s_mul_hi_u32 s11, s3, s12
	s_mul_i32 s12, s11, s7
	s_sub_i32 s3, s3, s12
	s_add_i32 s13, s11, 1
	s_sub_i32 s12, s3, s7
	s_cmp_ge_u32 s3, s7
	s_cselect_b32 s11, s13, s11
	s_cselect_b32 s3, s12, s3
	s_add_i32 s12, s11, 1
	s_cmp_ge_u32 s3, s7
	s_cselect_b32 s3, s12, s11
	s_xor_b32 s3, s3, s10
	s_sub_i32 s10, s3, s10
	s_mul_i32 s3, s10, s5
	s_sub_i32 s2, s2, s3
.Ldivjoin_1:
	s_add_i32 s16, s4, s2
	s_ashr_i32 s17, s16, 31
	s_lshl_b64 s[2:3], s[16:17], 2
	s_add_u32 s2, s33, s2
	s_addc_u32 s3, s50, s3
	v_mov_b32_e32 v0, 0
	global_load_dword v0, v0, s[2:3]
	s_waitcnt vmcnt(0)
	v_readfirstlane_b32 s40, v0

.LBB0_1209:
	s_add_i32 s71, s41, 1
	v_readlane_b32 s6, v252, 6
	s_mul_i32 s0, s71, s51
	v_readlane_b32 s7, v252, 7
	s_mul_hi_u32 s1, s71, s6
	s_add_i32 s1, s1, s0
	s_mul_i32 s0, s71, s6
	v_readlane_b32 s6, v252, 0
	v_readlane_b32 s7, v252, 1
	s_add_u32 s6, s0, s6
	s_addc_u32 s7, s1, s52
	v_cmp_ge_i64_e32 vcc, s[6:7], v[162:163]
	v_cmp_lt_i64_e64 s[0:1], s[6:7], v[162:163]
	s_cbranch_vccnz .LBB0_1211
	s_ashr_i32 s7, s6, 31
	s_lshr_b32 s7, s7, 29
	s_add_i32 s7, s6, s7
	s_ashr_i32 s34, s7, 3
	s_and_b32 s7, s7, -8
	s_sub_i32 s6, s6, s7
	s_cmp_lt_i32 s6, 0
	s_cselect_b32 s7, s66, s65
	s_mul_i32 s6, s6, s7
	s_add_i32 s6, s6, s34
	s_ashr_i32 s7, s6, 31
	s_lshr_b32 s7, s7, 25
	s_add_i32 s7, s6, s7
	s_ashr_i32 s34, s7, 7
	s_lshl_b32 s35, s34, 3
	s_sub_i32 s34, s31, s35
	s_min_i32 s36, s34, 8
	s_and_b32 s7, s7, 0xffffff80
	s_sub_i32 s6, s6, s7
	s_cmp_eq_u32 s36, 8
	s_cbranch_scc0 .Ldivslow_2
	s_ashr_i32 s34, s6, 3
	s_and_b32 s6, s6, 7
	s_branch .Ldivjoin_2
.Ldivslow_2:
	s_abs_i32 s34, s36
	v_cvt_f32_u32_e32 v0, s34
	s_sub_i32 s38, 0, s34
	v_rcp_iflag_f32_e32 v0, v0
	s_abs_i32 s7, s6
	s_xor_b32 s37, s6, s36
	s_ashr_i32 s37, s37, 31
	v_mul_f32_e32 v0, 0x4f7ffffe, v0
	v_cvt_u32_f32_e32 v0, v0
	s_nop 0
	v_readfirstlane_b32 s39, v0
	s_mul_i32 s38, s38, s39
	s_mul_hi_u32 s38, s39, s38
	s_add_i32 s39, s39, s38
	s_mul_hi_u32 s38, s7, s39
	s_mul_i32 s39, s38, s34
	s_sub_i32 s7, s7, s39
	s_add_i32 s44, s38, 1
	s_sub_i32 s39, s7, s34
	s_cmp_ge_u32 s7, s34
	s_cselect_b32 s38, s44, s38
	s_cselect_b32 s7, s39, s7
	s_add_i32 s39, s38, 1
	s_cmp_ge_u32 s7, s34
	s_cselect_b32 s7, s39, s38
	s_xor_b32 s7, s7, s37
	s_sub_i32 s34, s7, s37
	s_mul_i32 s7, s34, s36
	s_sub_i32 s6, s6, s7
.Ldivjoin_2:
	s_add_i32 s36, s35, s6
	s_ashr_i32 s37, s36, 31
	s_lshl_b32 s6, s36, 2
	s_add_i32 s6, s6, 0x21000
	v_mov_b32_e32 v0, s6
	ds_read_b32 v0, v0
	s_waitcnt lgkmcnt(0)
	v_readfirstlane_b32 s38, v0

.LBB0_1213:
	s_add_u32 s35, s42, 0x100
	s_addc_u32 s37, s43, 0
	s_mov_b32 s39, -2
	s_mov_b64 s[42:43], 0
	ds_read_b128 v[70:73], v190
	ds_read_b128 v[74:77], v190 offset:1024
	ds_read_b128 v[78:81], v190 offset:2048
	ds_read_b128 v[82:85], v190 offset:3072
	ds_read_b128 v[94:97], v191
	ds_read_b128 v[98:101], v191 offset:1024
	ds_read_b128 v[102:105], v191 offset:2048
	ds_read_b128 v[106:109], v191 offset:3072
	s_add_u32 s44, s42, 0x100
	s_addc_u32 s45, s43, 0
	s_add_u32 s48, s35, s42
	s_addc_u32 s49, s37, s43
	s_cmp_eq_u32 s39, 12
	s_cselect_b64 vcc, -1, 0
	s_and_b64 s[46:47], vcc, exec
	s_cselect_b32 s73, 0, s44
	s_cselect_b32 s72, 0, s45
	s_cselect_b32 s46, s0, s48
	s_cselect_b32 s47, s1, s49
	s_add_u32 s48, s14, s73
	s_addc_u32 s49, s15, s72
	s_add_i32 m0, s11, 0xc000
	s_add_u32 s42, s24, s42
	s_addc_u32 s43, s25, s43
	ds_read_b128 v[176:179], v192
	ds_read_b128 v[180:183], v192 offset:1024
	ds_read_b128 v[194:197], v192 offset:2048
	ds_read_b128 v[198:201], v192 offset:3072
	ds_read_b128 v[202:205], v192 offset:4096
	ds_read_b128 v[206:209], v192 offset:5120
	ds_read_b128 v[210:213], v192 offset:6144
	ds_read_b128 v[214:217], v192 offset:7168
	global_load_lds_dwordx4 v187, s[42:43]
	s_add_i32 m0, s11, 0xe000
	v_mov_b32_e32 v0, v172
	global_load_lds_dwordx4 v186, s[42:43]
	v_mov_b32_e32 v169, v173
	v_lshlrev_b32_e32 v184, 11, v0
	v_lshlrev_b32_e32 v185, 11, v169
	v_bfe_u32 v0, v0, 16, 16
	v_bfe_u32 v169, v169, 16, 16
	v_and_b32_e32 v184, 0x7fff800, v184
	v_and_b32_e32 v185, 0x7fff800, v185
	v_lshl_add_u32 v0, v0, 11, v175
	v_lshl_add_u32 v169, v169, 11, v175
	v_add_u32_e32 v184, v184, v175
	v_add_u32_e32 v185, v185, v175
	v_cndmask_b32_e32 v168, v168, v0, vcc
	v_cndmask_b32_e32 v186, v186, v169, vcc
	v_cndmask_b32_e32 v170, v170, v184, vcc
	v_cndmask_b32_e32 v187, v187, v185, vcc
	s_waitcnt vmcnt(24)
	s_waitcnt lgkmcnt(0)
	s_barrier
	s_setprio 1
	s_waitcnt lgkmcnt(0)
	v_mfma_i32_16x16x64_i8 v[158:161], v[70:73], v[176:179], 0
	v_mfma_i32_16x16x64_i8 v[150:153], v[78:81], v[176:179], 0
	v_mfma_i32_16x16x64_i8 v[142:145], v[70:73], v[194:197], 0
	v_mfma_i32_16x16x64_i8 v[134:137], v[78:81], v[194:197], 0
	v_mfma_i32_16x16x64_i8 v[126:129], v[70:73], v[202:205], 0
	v_mfma_i32_16x16x64_i8 v[118:121], v[78:81], v[202:205], 0
	v_mfma_i32_16x16x64_i8 v[110:113], v[70:73], v[210:213], 0
	v_mfma_i32_16x16x64_i8 v[86:89], v[78:81], v[210:213], 0
	v_mfma_i32_16x16x64_i8 v[158:161], v[74:77], v[180:183], v[158:161]
	v_mfma_i32_16x16x64_i8 v[150:153], v[82:85], v[180:183], v[150:153]
	v_mfma_i32_16x16x64_i8 v[142:145], v[74:77], v[198:201], v[142:145]
	v_mfma_i32_16x16x64_i8 v[134:137], v[82:85], v[198:201], v[134:137]
	v_mfma_i32_16x16x64_i8 v[126:129], v[74:77], v[206:209], v[126:129]
	v_mfma_i32_16x16x64_i8 v[118:121], v[82:85], v[206:209], v[118:121]
	v_mfma_i32_16x16x64_i8 v[110:113], v[74:77], v[214:217], v[110:113]
	v_mfma_i32_16x16x64_i8 v[86:89], v[82:85], v[214:217], v[86:89]
	s_setprio 0
	s_setprio 1
	v_mfma_i32_16x16x64_i8 v[154:157], v[94:97], v[176:179], 0
	v_mfma_i32_16x16x64_i8 v[146:149], v[102:105], v[176:179], 0
	v_mfma_i32_16x16x64_i8 v[138:141], v[94:97], v[194:197], 0
	v_mfma_i32_16x16x64_i8 v[130:133], v[102:105], v[194:197], 0
	v_mfma_i32_16x16x64_i8 v[122:125], v[94:97], v[202:205], 0
	v_mfma_i32_16x16x64_i8 v[114:117], v[102:105], v[202:205], 0
	v_mfma_i32_16x16x64_i8 v[90:93], v[94:97], v[210:213], 0
	v_mfma_i32_16x16x64_i8 v[66:69], v[102:105], v[210:213], 0
	v_mfma_i32_16x16x64_i8 v[154:157], v[98:101], v[180:183], v[154:157]
	v_mfma_i32_16x16x64_i8 v[146:149], v[106:109], v[180:183], v[146:149]
	v_mfma_i32_16x16x64_i8 v[138:141], v[98:101], v[198:201], v[138:141]
	v_mfma_i32_16x16x64_i8 v[130:133], v[106:109], v[198:201], v[130:133]
	v_mfma_i32_16x16x64_i8 v[122:125], v[98:101], v[206:209], v[122:125]
	v_mfma_i32_16x16x64_i8 v[114:117], v[106:109], v[206:209], v[114:117]
	v_mfma_i32_16x16x64_i8 v[90:93], v[98:101], v[214:217], v[90:93]
	v_mfma_i32_16x16x64_i8 v[66:69], v[106:109], v[214:217], v[66:69]
	s_setprio 0
	s_barrier
	s_add_i32 s42, s67, s57
	v_lshl_add_u64 v[184:185], s[46:47], 0, v[164:165]
	s_mov_b32 m0, s42
	ds_read_b128 v[176:179], v192 offset:16384
	ds_read_b128 v[180:183], v192 offset:17408
	ds_read_b128 v[194:197], v192 offset:18432
	ds_read_b128 v[198:201], v192 offset:19456
	ds_read_b128 v[202:205], v192 offset:20480
	ds_read_b128 v[206:209], v192 offset:21504
	ds_read_b128 v[210:213], v192 offset:22528
	ds_read_b128 v[214:217], v192 offset:23552
	global_load_lds_dwordx4 v[184:185], off
	s_add_i32 m0, s42, 0x2000
	s_add_u32 s42, s46, 0x40000
	v_lshl_add_u64 v[218:219], s[46:47], 0, v[166:167]
	s_addc_u32 s43, s47, 0
	s_add_i32 s72, s68, s57
	global_load_lds_dwordx4 v[218:219], off
	v_lshl_add_u64 v[220:221], s[42:43], 0, v[164:165]
	s_mov_b32 m0, s72
	v_mov_b32_e32 v169, v171
	global_load_lds_dwordx4 v[220:221], off
	v_lshl_add_u64 v[220:221], s[42:43], 0, v[166:167]
	s_add_i32 m0, s72, 0x2000
	v_lshl_add_u64 v[222:223], s[48:49], 0, v[168:169]
	global_load_lds_dwordx4 v[220:221], off
	s_mov_b32 m0, s11
	v_lshl_add_u64 v[220:221], s[48:49], 0, v[170:171]
	global_load_lds_dwordx4 v170, s[48:49]
	s_mov_b32 m0, s58
	s_nop 0
	global_load_lds_dwordx4 v168, s[48:49]
	s_waitcnt vmcnt(8)
	s_waitcnt lgkmcnt(0)
	s_barrier
	s_setprio 1
	s_waitcnt lgkmcnt(0)
	v_mfma_i32_16x16x64_i8 v[62:65], v[70:73], v[176:179], 0
	v_mfma_i32_16x16x64_i8 v[54:57], v[78:81], v[176:179], 0
	v_mfma_i32_16x16x64_i8 v[46:49], v[70:73], v[194:197], 0
	v_mfma_i32_16x16x64_i8 v[38:41], v[78:81], v[194:197], 0
	v_mfma_i32_16x16x64_i8 v[30:33], v[70:73], v[202:205], 0
	v_mfma_i32_16x16x64_i8 v[22:25], v[78:81], v[202:205], 0
	v_mfma_i32_16x16x64_i8 v[14:17], v[70:73], v[210:213], 0
	v_mfma_i32_16x16x64_i8 v[6:9], v[78:81], v[210:213], 0
	v_mfma_i32_16x16x64_i8 v[62:65], v[74:77], v[180:183], v[62:65]
	v_mfma_i32_16x16x64_i8 v[54:57], v[82:85], v[180:183], v[54:57]
	v_mfma_i32_16x16x64_i8 v[46:49], v[74:77], v[198:201], v[46:49]
	v_mfma_i32_16x16x64_i8 v[38:41], v[82:85], v[198:201], v[38:41]
	v_mfma_i32_16x16x64_i8 v[30:33], v[74:77], v[206:209], v[30:33]
	v_mfma_i32_16x16x64_i8 v[22:25], v[82:85], v[206:209], v[22:25]
	v_mfma_i32_16x16x64_i8 v[14:17], v[74:77], v[214:217], v[14:17]
	v_mfma_i32_16x16x64_i8 v[6:9], v[82:85], v[214:217], v[6:9]
	s_setprio 0
	s_setprio 1
	v_mfma_i32_16x16x64_i8 v[58:61], v[94:97], v[176:179], 0
	v_mfma_i32_16x16x64_i8 v[50:53], v[102:105], v[176:179], 0
	v_mfma_i32_16x16x64_i8 v[42:45], v[94:97], v[194:197], 0
	v_mfma_i32_16x16x64_i8 v[34:37], v[102:105], v[194:197], 0
	v_mfma_i32_16x16x64_i8 v[26:29], v[94:97], v[202:205], 0
	v_mfma_i32_16x16x64_i8 v[18:21], v[102:105], v[202:205], 0
	v_mfma_i32_16x16x64_i8 v[10:13], v[94:97], v[210:213], 0
	v_mfma_i32_16x16x64_i8 v[2:5], v[102:105], v[210:213], 0
	v_mfma_i32_16x16x64_i8 v[58:61], v[98:101], v[180:183], v[58:61]
	v_mfma_i32_16x16x64_i8 v[50:53], v[106:109], v[180:183], v[50:53]
	v_mfma_i32_16x16x64_i8 v[42:45], v[98:101], v[198:201], v[42:45]
	v_mfma_i32_16x16x64_i8 v[34:37], v[106:109], v[198:201], v[34:37]
	v_mfma_i32_16x16x64_i8 v[26:29], v[98:101], v[206:209], v[26:29]
	v_mfma_i32_16x16x64_i8 v[18:21], v[106:109], v[206:209], v[18:21]
	v_mfma_i32_16x16x64_i8 v[10:13], v[98:101], v[214:217], v[10:13]
	v_mfma_i32_16x16x64_i8 v[2:5], v[106:109], v[214:217], v[2:5]
	s_setprio 0
	s_barrier
	s_add_i32 s42, 0, 0x18000
	v_add_u32_e32 v0, s42, v189
	s_add_i32 s72, 0, 0x1c000
	ds_read_b128 v[70:73], v0
	ds_read_b128 v[74:77], v0 offset:1024
	ds_read_b128 v[78:81], v0 offset:2048
	ds_read_b128 v[82:85], v0 offset:3072
	v_add_u32_e32 v0, s72, v189
	ds_read_b128 v[94:97], v0
	ds_read_b128 v[98:101], v0 offset:1024
	ds_read_b128 v[102:105], v0 offset:2048
	ds_read_b128 v[106:109], v0 offset:3072
	s_mov_b32 m0, s59
	ds_read_b128 v[176:179], v192 offset:32768
	ds_read_b128 v[180:183], v192 offset:33792
	ds_read_b128 v[194:197], v192 offset:34816
	ds_read_b128 v[198:201], v192 offset:35840
	ds_read_b128 v[202:205], v192 offset:36864
	ds_read_b128 v[206:209], v192 offset:37888
	ds_read_b128 v[210:213], v192 offset:38912
	ds_read_b128 v[214:217], v192 offset:39936
	global_load_lds_dwordx4 v187, s[48:49]
	s_mov_b32 m0, s60
	s_nop 0
	global_load_lds_dwordx4 v186, s[48:49]
	s_waitcnt vmcnt(8)
	s_waitcnt lgkmcnt(0)
	s_barrier
	s_setprio 1
	s_waitcnt lgkmcnt(0)
	v_mfma_i32_16x16x64_i8 v[158:161], v[70:73], v[176:179], v[158:161]
	v_mfma_i32_16x16x64_i8 v[150:153], v[78:81], v[176:179], v[150:153]
	v_mfma_i32_16x16x64_i8 v[142:145], v[70:73], v[194:197], v[142:145]
	v_mfma_i32_16x16x64_i8 v[134:137], v[78:81], v[194:197], v[134:137]
	v_mfma_i32_16x16x64_i8 v[126:129], v[70:73], v[202:205], v[126:129]
	v_mfma_i32_16x16x64_i8 v[118:121], v[78:81], v[202:205], v[118:121]
	v_mfma_i32_16x16x64_i8 v[110:113], v[70:73], v[210:213], v[110:113]
	v_mfma_i32_16x16x64_i8 v[86:89], v[78:81], v[210:213], v[86:89]
	v_mfma_i32_16x16x64_i8 v[158:161], v[74:77], v[180:183], v[158:161]
	v_mfma_i32_16x16x64_i8 v[150:153], v[82:85], v[180:183], v[150:153]
	v_mfma_i32_16x16x64_i8 v[142:145], v[74:77], v[198:201], v[142:145]
	v_mfma_i32_16x16x64_i8 v[134:137], v[82:85], v[198:201], v[134:137]
	v_mfma_i32_16x16x64_i8 v[126:129], v[74:77], v[206:209], v[126:129]
	v_mfma_i32_16x16x64_i8 v[118:121], v[82:85], v[206:209], v[118:121]
	v_mfma_i32_16x16x64_i8 v[110:113], v[74:77], v[214:217], v[110:113]
	v_mfma_i32_16x16x64_i8 v[86:89], v[82:85], v[214:217], v[86:89]
	s_setprio 0
	s_setprio 1
	v_mfma_i32_16x16x64_i8 v[154:157], v[94:97], v[176:179], v[154:157]
	v_mfma_i32_16x16x64_i8 v[146:149], v[102:105], v[176:179], v[146:149]
	v_mfma_i32_16x16x64_i8 v[138:141], v[94:97], v[194:197], v[138:141]
	v_mfma_i32_16x16x64_i8 v[130:133], v[102:105], v[194:197], v[130:133]
	v_mfma_i32_16x16x64_i8 v[122:125], v[94:97], v[202:205], v[122:125]
	v_mfma_i32_16x16x64_i8 v[114:117], v[102:105], v[202:205], v[114:117]
	v_mfma_i32_16x16x64_i8 v[90:93], v[94:97], v[210:213], v[90:93]
	v_mfma_i32_16x16x64_i8 v[66:69], v[102:105], v[210:213], v[66:69]
	v_mfma_i32_16x16x64_i8 v[154:157], v[98:101], v[180:183], v[154:157]
	v_mfma_i32_16x16x64_i8 v[146:149], v[106:109], v[180:183], v[146:149]
	v_mfma_i32_16x16x64_i8 v[138:141], v[98:101], v[198:201], v[138:141]
	v_mfma_i32_16x16x64_i8 v[130:133], v[106:109], v[198:201], v[130:133]
	v_mfma_i32_16x16x64_i8 v[122:125], v[98:101], v[206:209], v[122:125]
	v_mfma_i32_16x16x64_i8 v[114:117], v[106:109], v[206:209], v[114:117]
	v_mfma_i32_16x16x64_i8 v[90:93], v[98:101], v[214:217], v[90:93]
	v_mfma_i32_16x16x64_i8 v[66:69], v[106:109], v[214:217], v[66:69]
	s_setprio 0
	s_barrier
	s_add_i32 s42, s42, s57
	v_lshl_add_u64 v[184:185], v[184:185], 0, s[22:23]
	s_mov_b32 m0, s42
	ds_read_b128 v[176:179], v192 offset:49152
	ds_read_b128 v[180:183], v192 offset:50176
	ds_read_b128 v[194:197], v192 offset:51200
	ds_read_b128 v[198:201], v192 offset:52224
	ds_read_b128 v[202:205], v192 offset:53248
	ds_read_b128 v[206:209], v192 offset:54272
	ds_read_b128 v[210:213], v192 offset:55296
	ds_read_b128 v[214:217], v192 offset:56320
	global_load_lds_dwordx4 v[184:185], off
	s_add_i32 m0, s42, 0x2000
	s_add_u32 s42, s46, 0x40080
	v_lshl_add_u64 v[184:185], v[218:219], 0, s[22:23]
	s_addc_u32 s43, s47, 0
	s_add_i32 s46, s72, s57
	global_load_lds_dwordx4 v[184:185], off
	v_lshl_add_u64 v[184:185], s[42:43], 0, v[164:165]
	s_mov_b32 m0, s46
	s_nop 0
	global_load_lds_dwordx4 v[184:185], off
	v_lshl_add_u64 v[184:185], s[42:43], 0, v[166:167]
	s_add_i32 m0, s46, 0x2000
	s_nop 0
	global_load_lds_dwordx4 v[184:185], off
	v_lshl_add_u64 v[184:185], v[220:221], 0, s[22:23]
	s_mov_b32 m0, s63
	s_nop 0
	global_load_lds_dwordx4 v[184:185], off
	v_lshl_add_u64 v[184:185], v[222:223], 0, s[22:23]
	s_mov_b32 m0, s64
	s_nop 0
	global_load_lds_dwordx4 v[184:185], off
	s_waitcnt vmcnt(8)
	s_waitcnt lgkmcnt(0)
	s_barrier
	s_setprio 1
	s_waitcnt lgkmcnt(0)
	v_mfma_i32_16x16x64_i8 v[62:65], v[70:73], v[176:179], v[62:65]
	v_mfma_i32_16x16x64_i8 v[54:57], v[78:81], v[176:179], v[54:57]
	v_mfma_i32_16x16x64_i8 v[46:49], v[70:73], v[194:197], v[46:49]
	v_mfma_i32_16x16x64_i8 v[38:41], v[78:81], v[194:197], v[38:41]
	v_mfma_i32_16x16x64_i8 v[30:33], v[70:73], v[202:205], v[30:33]
	v_mfma_i32_16x16x64_i8 v[22:25], v[78:81], v[202:205], v[22:25]
	v_mfma_i32_16x16x64_i8 v[14:17], v[70:73], v[210:213], v[14:17]
	v_mfma_i32_16x16x64_i8 v[6:9], v[78:81], v[210:213], v[6:9]
	v_mfma_i32_16x16x64_i8 v[62:65], v[74:77], v[180:183], v[62:65]
	v_mfma_i32_16x16x64_i8 v[54:57], v[82:85], v[180:183], v[54:57]
	v_mfma_i32_16x16x64_i8 v[46:49], v[74:77], v[198:201], v[46:49]
	v_mfma_i32_16x16x64_i8 v[38:41], v[82:85], v[198:201], v[38:41]
	v_mfma_i32_16x16x64_i8 v[30:33], v[74:77], v[206:209], v[30:33]
	v_mfma_i32_16x16x64_i8 v[22:25], v[82:85], v[206:209], v[22:25]
	v_mfma_i32_16x16x64_i8 v[14:17], v[74:77], v[214:217], v[14:17]
	v_mfma_i32_16x16x64_i8 v[6:9], v[82:85], v[214:217], v[6:9]
	s_setprio 0
	s_setprio 1
	v_mfma_i32_16x16x64_i8 v[58:61], v[94:97], v[176:179], v[58:61]
	v_mfma_i32_16x16x64_i8 v[50:53], v[102:105], v[176:179], v[50:53]
	v_mfma_i32_16x16x64_i8 v[42:45], v[94:97], v[194:197], v[42:45]
	v_mfma_i32_16x16x64_i8 v[34:37], v[102:105], v[194:197], v[34:37]
	v_mfma_i32_16x16x64_i8 v[26:29], v[94:97], v[202:205], v[26:29]
	v_mfma_i32_16x16x64_i8 v[18:21], v[102:105], v[202:205], v[18:21]
	v_mfma_i32_16x16x64_i8 v[10:13], v[94:97], v[210:213], v[10:13]
	v_mfma_i32_16x16x64_i8 v[2:5], v[102:105], v[210:213], v[2:5]
	v_mfma_i32_16x16x64_i8 v[58:61], v[98:101], v[180:183], v[58:61]
	v_mfma_i32_16x16x64_i8 v[50:53], v[106:109], v[180:183], v[50:53]
	v_mfma_i32_16x16x64_i8 v[42:45], v[98:101], v[198:201], v[42:45]
	v_mfma_i32_16x16x64_i8 v[34:37], v[106:109], v[198:201], v[34:37]
	v_mfma_i32_16x16x64_i8 v[26:29], v[98:101], v[206:209], v[26:29]
	v_mfma_i32_16x16x64_i8 v[18:21], v[106:109], v[206:209], v[18:21]
	v_mfma_i32_16x16x64_i8 v[10:13], v[98:101], v[214:217], v[10:13]
	v_mfma_i32_16x16x64_i8 v[2:5], v[106:109], v[214:217], v[2:5]
	s_setprio 0
	s_barrier
	s_add_i32 s39, s39, 2
	s_cmp_gt_u32 s39, 13
	s_mov_b64 s[42:43], s[44:45]
	s_cbranch_scc0 .LBB0_1214
	s_branch .Lkexit_1214
	s_nop 0
	s_nop 0
	s_nop 0
	s_nop 0
	s_nop 0
	s_nop 0
	s_nop 0
	s_nop 0
	s_nop 0
	s_nop 0
	s_nop 0
	s_nop 0
	s_nop 0
	s_nop 0
	s_nop 0
	s_nop 0
	s_nop 0
.LBB0_1214:
	ds_read_b128 v[70:73], v190
	ds_read_b128 v[74:77], v190 offset:1024
	ds_read_b128 v[78:81], v190 offset:2048
	ds_read_b128 v[82:85], v190 offset:3072
	ds_read_b128 v[94:97], v191
	ds_read_b128 v[98:101], v191 offset:1024
	ds_read_b128 v[102:105], v191 offset:2048
	ds_read_b128 v[106:109], v191 offset:3072
	s_add_u32 s44, s42, 0x100
	s_addc_u32 s45, s43, 0
	s_add_u32 s48, s35, s42
	s_addc_u32 s49, s37, s43
	s_cmp_eq_u32 s39, 12
	s_cselect_b64 vcc, -1, 0
	s_and_b64 s[46:47], vcc, exec
	s_cselect_b32 s73, 0, s44
	s_cselect_b32 s72, 0, s45
	s_cselect_b32 s46, s0, s48
	s_cselect_b32 s47, s1, s49
	s_add_u32 s48, s14, s73
	s_addc_u32 s49, s15, s72
	s_add_i32 m0, s11, 0xc000
	s_add_u32 s42, s24, s42
	s_addc_u32 s43, s25, s43
	ds_read_b128 v[176:179], v192
	ds_read_b128 v[180:183], v192 offset:1024
	ds_read_b128 v[194:197], v192 offset:2048
	ds_read_b128 v[198:201], v192 offset:3072
	ds_read_b128 v[202:205], v192 offset:4096
	ds_read_b128 v[206:209], v192 offset:5120
	ds_read_b128 v[210:213], v192 offset:6144
	ds_read_b128 v[214:217], v192 offset:7168
	global_load_lds_dwordx4 v187, s[42:43]
	s_add_i32 m0, s11, 0xe000
	v_mov_b32_e32 v0, v172
	global_load_lds_dwordx4 v186, s[42:43]
	v_mov_b32_e32 v169, v173
	v_lshlrev_b32_e32 v184, 11, v0
	v_lshlrev_b32_e32 v185, 11, v169
	v_bfe_u32 v0, v0, 16, 16
	v_bfe_u32 v169, v169, 16, 16
	v_and_b32_e32 v184, 0x7fff800, v184
	v_and_b32_e32 v185, 0x7fff800, v185
	v_lshl_add_u32 v0, v0, 11, v175
	v_lshl_add_u32 v169, v169, 11, v175
	v_add_u32_e32 v184, v184, v175
	v_add_u32_e32 v185, v185, v175
	v_cndmask_b32_e32 v168, v168, v0, vcc
	v_cndmask_b32_e32 v186, v186, v169, vcc
	v_cndmask_b32_e32 v170, v170, v184, vcc
	v_cndmask_b32_e32 v187, v187, v185, vcc
	s_waitcnt vmcnt(8)
	s_waitcnt lgkmcnt(0)
	s_barrier
	s_setprio 1
	s_waitcnt lgkmcnt(0)
	v_mfma_i32_16x16x64_i8 v[158:161], v[70:73], v[176:179], v[158:161]
	v_mfma_i32_16x16x64_i8 v[150:153], v[78:81], v[176:179], v[150:153]
	v_mfma_i32_16x16x64_i8 v[142:145], v[70:73], v[194:197], v[142:145]
	v_mfma_i32_16x16x64_i8 v[134:137], v[78:81], v[194:197], v[134:137]
	v_mfma_i32_16x16x64_i8 v[126:129], v[70:73], v[202:205], v[126:129]
	v_mfma_i32_16x16x64_i8 v[118:121], v[78:81], v[202:205], v[118:121]
	v_mfma_i32_16x16x64_i8 v[110:113], v[70:73], v[210:213], v[110:113]
	v_mfma_i32_16x16x64_i8 v[86:89], v[78:81], v[210:213], v[86:89]
	v_mfma_i32_16x16x64_i8 v[158:161], v[74:77], v[180:183], v[158:161]
	v_mfma_i32_16x16x64_i8 v[150:153], v[82:85], v[180:183], v[150:153]
	v_mfma_i32_16x16x64_i8 v[142:145], v[74:77], v[198:201], v[142:145]
	v_mfma_i32_16x16x64_i8 v[134:137], v[82:85], v[198:201], v[134:137]
	v_mfma_i32_16x16x64_i8 v[126:129], v[74:77], v[206:209], v[126:129]
	v_mfma_i32_16x16x64_i8 v[118:121], v[82:85], v[206:209], v[118:121]
	v_mfma_i32_16x16x64_i8 v[110:113], v[74:77], v[214:217], v[110:113]
	v_mfma_i32_16x16x64_i8 v[86:89], v[82:85], v[214:217], v[86:89]
	s_setprio 0
	s_setprio 1
	v_mfma_i32_16x16x64_i8 v[154:157], v[94:97], v[176:179], v[154:157]
	v_mfma_i32_16x16x64_i8 v[146:149], v[102:105], v[176:179], v[146:149]
	v_mfma_i32_16x16x64_i8 v[138:141], v[94:97], v[194:197], v[138:141]
	v_mfma_i32_16x16x64_i8 v[130:133], v[102:105], v[194:197], v[130:133]
	v_mfma_i32_16x16x64_i8 v[122:125], v[94:97], v[202:205], v[122:125]
	v_mfma_i32_16x16x64_i8 v[114:117], v[102:105], v[202:205], v[114:117]
	v_mfma_i32_16x16x64_i8 v[90:93], v[94:97], v[210:213], v[90:93]
	v_mfma_i32_16x16x64_i8 v[66:69], v[102:105], v[210:213], v[66:69]
	v_mfma_i32_16x16x64_i8 v[154:157], v[98:101], v[180:183], v[154:157]
	v_mfma_i32_16x16x64_i8 v[146:149], v[106:109], v[180:183], v[146:149]
	v_mfma_i32_16x16x64_i8 v[138:141], v[98:101], v[198:201], v[138:141]
	v_mfma_i32_16x16x64_i8 v[130:133], v[106:109], v[198:201], v[130:133]
	v_mfma_i32_16x16x64_i8 v[122:125], v[98:101], v[206:209], v[122:125]
	v_mfma_i32_16x16x64_i8 v[114:117], v[106:109], v[206:209], v[114:117]
	v_mfma_i32_16x16x64_i8 v[90:93], v[98:101], v[214:217], v[90:93]
	v_mfma_i32_16x16x64_i8 v[66:69], v[106:109], v[214:217], v[66:69]
	s_setprio 0
	s_barrier
	s_add_i32 s42, s67, s57
	v_lshl_add_u64 v[184:185], s[46:47], 0, v[164:165]
	s_mov_b32 m0, s42
	ds_read_b128 v[176:179], v192 offset:16384
	ds_read_b128 v[180:183], v192 offset:17408
	ds_read_b128 v[194:197], v192 offset:18432
	ds_read_b128 v[198:201], v192 offset:19456
	ds_read_b128 v[202:205], v192 offset:20480
	ds_read_b128 v[206:209], v192 offset:21504
	ds_read_b128 v[210:213], v192 offset:22528
	ds_read_b128 v[214:217], v192 offset:23552
	global_load_lds_dwordx4 v[184:185], off
	s_add_i32 m0, s42, 0x2000
	s_add_u32 s42, s46, 0x40000
	v_lshl_add_u64 v[218:219], s[46:47], 0, v[166:167]
	s_addc_u32 s43, s47, 0
	s_add_i32 s72, s68, s57
	global_load_lds_dwordx4 v[218:219], off
	v_lshl_add_u64 v[220:221], s[42:43], 0, v[164:165]
	s_mov_b32 m0, s72
	v_mov_b32_e32 v169, v171
	global_load_lds_dwordx4 v[220:221], off
	v_lshl_add_u64 v[220:221], s[42:43], 0, v[166:167]
	s_add_i32 m0, s72, 0x2000
	v_lshl_add_u64 v[222:223], s[48:49], 0, v[168:169]
	global_load_lds_dwordx4 v[220:221], off
	s_mov_b32 m0, s11
	v_lshl_add_u64 v[220:221], s[48:49], 0, v[170:171]
	global_load_lds_dwordx4 v170, s[48:49]
	s_mov_b32 m0, s58
	s_nop 0
	global_load_lds_dwordx4 v168, s[48:49]
	s_waitcnt vmcnt(8)
	s_waitcnt lgkmcnt(0)
	s_barrier
	s_setprio 1
	s_waitcnt lgkmcnt(0)
	v_mfma_i32_16x16x64_i8 v[62:65], v[70:73], v[176:179], v[62:65]
	v_mfma_i32_16x16x64_i8 v[54:57], v[78:81], v[176:179], v[54:57]
	v_mfma_i32_16x16x64_i8 v[46:49], v[70:73], v[194:197], v[46:49]
	v_mfma_i32_16x16x64_i8 v[38:41], v[78:81], v[194:197], v[38:41]
	v_mfma_i32_16x16x64_i8 v[30:33], v[70:73], v[202:205], v[30:33]
	v_mfma_i32_16x16x64_i8 v[22:25], v[78:81], v[202:205], v[22:25]
	v_mfma_i32_16x16x64_i8 v[14:17], v[70:73], v[210:213], v[14:17]
	v_mfma_i32_16x16x64_i8 v[6:9], v[78:81], v[210:213], v[6:9]
	v_mfma_i32_16x16x64_i8 v[62:65], v[74:77], v[180:183], v[62:65]
	v_mfma_i32_16x16x64_i8 v[54:57], v[82:85], v[180:183], v[54:57]
	v_mfma_i32_16x16x64_i8 v[46:49], v[74:77], v[198:201], v[46:49]
	v_mfma_i32_16x16x64_i8 v[38:41], v[82:85], v[198:201], v[38:41]
	v_mfma_i32_16x16x64_i8 v[30:33], v[74:77], v[206:209], v[30:33]
	v_mfma_i32_16x16x64_i8 v[22:25], v[82:85], v[206:209], v[22:25]
	v_mfma_i32_16x16x64_i8 v[14:17], v[74:77], v[214:217], v[14:17]
	v_mfma_i32_16x16x64_i8 v[6:9], v[82:85], v[214:217], v[6:9]
	s_setprio 0
	s_setprio 1
	v_mfma_i32_16x16x64_i8 v[58:61], v[94:97], v[176:179], v[58:61]
	v_mfma_i32_16x16x64_i8 v[50:53], v[102:105], v[176:179], v[50:53]
	v_mfma_i32_16x16x64_i8 v[42:45], v[94:97], v[194:197], v[42:45]
	v_mfma_i32_16x16x64_i8 v[34:37], v[102:105], v[194:197], v[34:37]
	v_mfma_i32_16x16x64_i8 v[26:29], v[94:97], v[202:205], v[26:29]
	v_mfma_i32_16x16x64_i8 v[18:21], v[102:105], v[202:205], v[18:21]
	v_mfma_i32_16x16x64_i8 v[10:13], v[94:97], v[210:213], v[10:13]
	v_mfma_i32_16x16x64_i8 v[2:5], v[102:105], v[210:213], v[2:5]
	v_mfma_i32_16x16x64_i8 v[58:61], v[98:101], v[180:183], v[58:61]
	v_mfma_i32_16x16x64_i8 v[50:53], v[106:109], v[180:183], v[50:53]
	v_mfma_i32_16x16x64_i8 v[42:45], v[98:101], v[198:201], v[42:45]
	v_mfma_i32_16x16x64_i8 v[34:37], v[106:109], v[198:201], v[34:37]
	v_mfma_i32_16x16x64_i8 v[26:29], v[98:101], v[206:209], v[26:29]
	v_mfma_i32_16x16x64_i8 v[18:21], v[106:109], v[206:209], v[18:21]
	v_mfma_i32_16x16x64_i8 v[10:13], v[98:101], v[214:217], v[10:13]
	v_mfma_i32_16x16x64_i8 v[2:5], v[106:109], v[214:217], v[2:5]
	s_setprio 0
	s_barrier
	s_add_i32 s42, 0, 0x18000
	v_add_u32_e32 v0, s42, v189
	s_add_i32 s72, 0, 0x1c000
	ds_read_b128 v[70:73], v0
	ds_read_b128 v[74:77], v0 offset:1024
	ds_read_b128 v[78:81], v0 offset:2048
	ds_read_b128 v[82:85], v0 offset:3072
	v_add_u32_e32 v0, s72, v189
	ds_read_b128 v[94:97], v0
	ds_read_b128 v[98:101], v0 offset:1024
	ds_read_b128 v[102:105], v0 offset:2048
	ds_read_b128 v[106:109], v0 offset:3072
	s_mov_b32 m0, s59
	ds_read_b128 v[176:179], v192 offset:32768
	ds_read_b128 v[180:183], v192 offset:33792
	ds_read_b128 v[194:197], v192 offset:34816
	ds_read_b128 v[198:201], v192 offset:35840
	ds_read_b128 v[202:205], v192 offset:36864
	ds_read_b128 v[206:209], v192 offset:37888
	ds_read_b128 v[210:213], v192 offset:38912
	ds_read_b128 v[214:217], v192 offset:39936
	global_load_lds_dwordx4 v187, s[48:49]
	s_mov_b32 m0, s60
	s_nop 0
	global_load_lds_dwordx4 v186, s[48:49]
	s_waitcnt vmcnt(8)
	s_waitcnt lgkmcnt(0)
	s_barrier
	s_setprio 1
	s_waitcnt lgkmcnt(0)
	v_mfma_i32_16x16x64_i8 v[158:161], v[70:73], v[176:179], v[158:161]
	v_mfma_i32_16x16x64_i8 v[150:153], v[78:81], v[176:179], v[150:153]
	v_mfma_i32_16x16x64_i8 v[142:145], v[70:73], v[194:197], v[142:145]
	v_mfma_i32_16x16x64_i8 v[134:137], v[78:81], v[194:197], v[134:137]
	v_mfma_i32_16x16x64_i8 v[126:129], v[70:73], v[202:205], v[126:129]
	v_mfma_i32_16x16x64_i8 v[118:121], v[78:81], v[202:205], v[118:121]
	v_mfma_i32_16x16x64_i8 v[110:113], v[70:73], v[210:213], v[110:113]
	v_mfma_i32_16x16x64_i8 v[86:89], v[78:81], v[210:213], v[86:89]
	v_mfma_i32_16x16x64_i8 v[158:161], v[74:77], v[180:183], v[158:161]
	v_mfma_i32_16x16x64_i8 v[150:153], v[82:85], v[180:183], v[150:153]
	v_mfma_i32_16x16x64_i8 v[142:145], v[74:77], v[198:201], v[142:145]
	v_mfma_i32_16x16x64_i8 v[134:137], v[82:85], v[198:201], v[134:137]
	v_mfma_i32_16x16x64_i8 v[126:129], v[74:77], v[206:209], v[126:129]
	v_mfma_i32_16x16x64_i8 v[118:121], v[82:85], v[206:209], v[118:121]
	v_mfma_i32_16x16x64_i8 v[110:113], v[74:77], v[214:217], v[110:113]
	v_mfma_i32_16x16x64_i8 v[86:89], v[82:85], v[214:217], v[86:89]
	s_setprio 0
	s_setprio 1
	v_mfma_i32_16x16x64_i8 v[154:157], v[94:97], v[176:179], v[154:157]
	v_mfma_i32_16x16x64_i8 v[146:149], v[102:105], v[176:179], v[146:149]
	v_mfma_i32_16x16x64_i8 v[138:141], v[94:97], v[194:197], v[138:141]
	v_mfma_i32_16x16x64_i8 v[130:133], v[102:105], v[194:197], v[130:133]
	v_mfma_i32_16x16x64_i8 v[122:125], v[94:97], v[202:205], v[122:125]
	v_mfma_i32_16x16x64_i8 v[114:117], v[102:105], v[202:205], v[114:117]
	v_mfma_i32_16x16x64_i8 v[90:93], v[94:97], v[210:213], v[90:93]
	v_mfma_i32_16x16x64_i8 v[66:69], v[102:105], v[210:213], v[66:69]
	v_mfma_i32_16x16x64_i8 v[154:157], v[98:101], v[180:183], v[154:157]
	v_mfma_i32_16x16x64_i8 v[146:149], v[106:109], v[180:183], v[146:149]
	v_mfma_i32_16x16x64_i8 v[138:141], v[98:101], v[198:201], v[138:141]
	v_mfma_i32_16x16x64_i8 v[130:133], v[106:109], v[198:201], v[130:133]
	v_mfma_i32_16x16x64_i8 v[122:125], v[98:101], v[206:209], v[122:125]
	v_mfma_i32_16x16x64_i8 v[114:117], v[106:109], v[206:209], v[114:117]
	v_mfma_i32_16x16x64_i8 v[90:93], v[98:101], v[214:217], v[90:93]
	v_mfma_i32_16x16x64_i8 v[66:69], v[106:109], v[214:217], v[66:69]
	s_setprio 0
	s_barrier
	s_add_i32 s42, s42, s57
	v_lshl_add_u64 v[184:185], v[184:185], 0, s[22:23]
	s_mov_b32 m0, s42
	ds_read_b128 v[176:179], v192 offset:49152
	ds_read_b128 v[180:183], v192 offset:50176
	ds_read_b128 v[194:197], v192 offset:51200
	ds_read_b128 v[198:201], v192 offset:52224
	ds_read_b128 v[202:205], v192 offset:53248
	ds_read_b128 v[206:209], v192 offset:54272
	ds_read_b128 v[210:213], v192 offset:55296
	ds_read_b128 v[214:217], v192 offset:56320
	global_load_lds_dwordx4 v[184:185], off
	s_add_i32 m0, s42, 0x2000
	s_add_u32 s42, s46, 0x40080
	v_lshl_add_u64 v[184:185], v[218:219], 0, s[22:23]
	s_addc_u32 s43, s47, 0
	s_add_i32 s46, s72, s57
	global_load_lds_dwordx4 v[184:185], off
	v_lshl_add_u64 v[184:185], s[42:43], 0, v[164:165]
	s_mov_b32 m0, s46
	s_nop 0
	global_load_lds_dwordx4 v[184:185], off
	v_lshl_add_u64 v[184:185], s[42:43], 0, v[166:167]
	s_add_i32 m0, s46, 0x2000
	s_nop 0
	global_load_lds_dwordx4 v[184:185], off
	v_lshl_add_u64 v[184:185], v[220:221], 0, s[22:23]
	s_mov_b32 m0, s63
	s_nop 0
	global_load_lds_dwordx4 v[184:185], off
	v_lshl_add_u64 v[184:185], v[222:223], 0, s[22:23]
	s_mov_b32 m0, s64
	s_nop 0
	global_load_lds_dwordx4 v[184:185], off
	s_waitcnt vmcnt(8)
	s_waitcnt lgkmcnt(0)
	s_barrier
	s_setprio 1
	s_waitcnt lgkmcnt(0)
	v_mfma_i32_16x16x64_i8 v[62:65], v[70:73], v[176:179], v[62:65]
	v_mfma_i32_16x16x64_i8 v[54:57], v[78:81], v[176:179], v[54:57]
	v_mfma_i32_16x16x64_i8 v[46:49], v[70:73], v[194:197], v[46:49]
	v_mfma_i32_16x16x64_i8 v[38:41], v[78:81], v[194:197], v[38:41]
	v_mfma_i32_16x16x64_i8 v[30:33], v[70:73], v[202:205], v[30:33]
	v_mfma_i32_16x16x64_i8 v[22:25], v[78:81], v[202:205], v[22:25]
	v_mfma_i32_16x16x64_i8 v[14:17], v[70:73], v[210:213], v[14:17]
	v_mfma_i32_16x16x64_i8 v[6:9], v[78:81], v[210:213], v[6:9]
	v_mfma_i32_16x16x64_i8 v[62:65], v[74:77], v[180:183], v[62:65]
	v_mfma_i32_16x16x64_i8 v[54:57], v[82:85], v[180:183], v[54:57]
	v_mfma_i32_16x16x64_i8 v[46:49], v[74:77], v[198:201], v[46:49]
	v_mfma_i32_16x16x64_i8 v[38:41], v[82:85], v[198:201], v[38:41]
	v_mfma_i32_16x16x64_i8 v[30:33], v[74:77], v[206:209], v[30:33]
	v_mfma_i32_16x16x64_i8 v[22:25], v[82:85], v[206:209], v[22:25]
	v_mfma_i32_16x16x64_i8 v[14:17], v[74:77], v[214:217], v[14:17]
	v_mfma_i32_16x16x64_i8 v[6:9], v[82:85], v[214:217], v[6:9]
	s_setprio 0
	s_setprio 1
	v_mfma_i32_16x16x64_i8 v[58:61], v[94:97], v[176:179], v[58:61]
	v_mfma_i32_16x16x64_i8 v[50:53], v[102:105], v[176:179], v[50:53]
	v_mfma_i32_16x16x64_i8 v[42:45], v[94:97], v[194:197], v[42:45]
	v_mfma_i32_16x16x64_i8 v[34:37], v[102:105], v[194:197], v[34:37]
	v_mfma_i32_16x16x64_i8 v[26:29], v[94:97], v[202:205], v[26:29]
	v_mfma_i32_16x16x64_i8 v[18:21], v[102:105], v[202:205], v[18:21]
	v_mfma_i32_16x16x64_i8 v[10:13], v[94:97], v[210:213], v[10:13]
	v_mfma_i32_16x16x64_i8 v[2:5], v[102:105], v[210:213], v[2:5]
	v_mfma_i32_16x16x64_i8 v[58:61], v[98:101], v[180:183], v[58:61]
	v_mfma_i32_16x16x64_i8 v[50:53], v[106:109], v[180:183], v[50:53]
	v_mfma_i32_16x16x64_i8 v[42:45], v[98:101], v[198:201], v[42:45]
	v_mfma_i32_16x16x64_i8 v[34:37], v[106:109], v[198:201], v[34:37]
	v_mfma_i32_16x16x64_i8 v[26:29], v[98:101], v[206:209], v[26:29]
	v_mfma_i32_16x16x64_i8 v[18:21], v[106:109], v[206:209], v[18:21]
	v_mfma_i32_16x16x64_i8 v[10:13], v[98:101], v[214:217], v[10:13]
	v_mfma_i32_16x16x64_i8 v[2:5], v[106:109], v[214:217], v[2:5]
	s_setprio 0
	s_barrier
	s_add_i32 s39, s39, 2
	s_cmp_gt_u32 s39, 13
	s_mov_b64 s[42:43], s[44:45]
	s_cbranch_scc0 .LBB0_1214

.LBB0_1217:
	s_add_i32 s35, s41, 2
	v_readlane_b32 s42, v252, 6
	s_mul_i32 s37, s35, s51
	v_readlane_b32 s43, v252, 7
	s_mul_hi_u32 s39, s35, s42
	s_add_i32 s39, s39, s37
	s_mul_i32 s35, s35, s42
	v_readlane_b32 s42, v252, 0
	v_readlane_b32 s43, v252, 1
	s_add_u32 s42, s35, s42
	s_addc_u32 s43, s39, s52
	v_cmp_ge_i64_e32 vcc, s[42:43], v[162:163]
	s_mov_b32 s44, s16
	s_cbranch_vccnz .LBB0_1219
	s_ashr_i32 s35, s42, 31
	s_lshr_b32 s35, s35, 29
	s_add_i32 s35, s42, s35
	s_ashr_i32 s37, s35, 3
	s_and_b32 s35, s35, -8
	s_sub_i32 s35, s42, s35
	s_cmp_lt_i32 s35, 0
	s_cselect_b32 s39, s66, s65
	s_mul_i32 s35, s35, s39
	s_add_i32 s35, s35, s37
	s_ashr_i32 s37, s35, 31
	s_lshr_b32 s37, s37, 25
	s_add_i32 s37, s35, s37
	s_ashr_i32 s39, s37, 7
	s_lshl_b32 s39, s39, 3
	s_sub_i32 s41, s31, s39
	s_min_i32 s41, s41, 8
	s_and_b32 s37, s37, 0xffffff80
	s_sub_i32 s35, s35, s37
	s_ashr_i32 s37, s35, 31
	s_abs_i32 s35, s35
	s_cmp_eq_u32 s41, 8
	s_cbranch_scc0 .Ldivslow_5
	s_and_b32 s35, s35, 7
	s_branch .Ldivjoin_5
.Ldivslow_5:
	s_abs_i32 s41, s41
	v_cvt_f32_u32_e32 v0, s41
	s_sub_i32 s42, 0, s41
	v_rcp_iflag_f32_e32 v0, v0
	s_nop 0
	v_mul_f32_e32 v0, 0x4f7ffffe, v0
	v_cvt_u32_f32_e32 v0, v0
	s_nop 0
	v_readfirstlane_b32 s43, v0
	s_mul_i32 s42, s42, s43
	s_mul_hi_u32 s42, s43, s42
	s_add_i32 s43, s43, s42
	s_mul_hi_u32 s42, s35, s43
	s_mul_i32 s42, s42, s41
	s_sub_i32 s35, s35, s42
	s_sub_i32 s42, s35, s41
	s_cmp_ge_u32 s35, s41
	s_cselect_b32 s35, s42, s35
	s_sub_i32 s42, s35, s41
	s_cmp_ge_u32 s35, s41
	s_cselect_b32 s35, s42, s35
.Ldivjoin_5:
	s_xor_b32 s35, s35, s37
	s_sub_i32 s35, s35, s37
	s_add_i32 s44, s39, s35

.LBB0_1235:
	s_or_b64 exec, exec, s[40:41]
	v_rcp_f32_e32 v0, v8
	v_cmp_lt_f32_e32 vcc, 0, v8
	v_mul_f32_e32 v0, 0x42fe0000, v0
	s_nop 0
	v_cndmask_b32_e32 v0, 0, v0, vcc
	v_pk_mul_f32 v[8:9], v[10:11], v[0:1] op_sel_hi:[1,0]
	v_pk_mul_f32 v[10:11], v[12:13], v[0:1] op_sel_hi:[1,0]
	v_pk_mul_f32 v[2:3], v[2:3], v[0:1] op_sel_hi:[1,0]
	v_pk_mul_f32 v[6:7], v[6:7], v[0:1] op_sel_hi:[1,0]
	v_add_f32_e32 v0, 0x4b400000, v8
	v_add_f32_e32 v8, 0x4b400000, v9
	v_add_f32_e32 v9, 0x4b400000, v10
	v_add_f32_e32 v10, 0x4b400000, v11
	v_perm_b32 v0, v8, v0, s70
	v_perm_b32 v8, v10, v9, s70
	v_lshl_or_b32 v8, v8, 16, v0
	v_add_f32_e32 v0, 0x4b400000, v2
	v_add_f32_e32 v2, 0x4b400000, v3
	v_add_f32_e32 v3, 0x4b400000, v6
	v_add_f32_e32 v6, 0x4b400000, v7
	v_perm_b32 v0, v2, v0, s70
	v_perm_b32 v2, v6, v3, s70
	v_lshl_or_b32 v9, v2, 16, v0
	v_lshlrev_b64 v[2:3], 11, v[4:5]
	v_lshl_add_u64 v[2:3], s[2:3], 0, v[2:3]
	v_lshl_add_u64 v[2:3], v[2:3], 0, v[176:177]
	s_and_b64 vcc, exec, s[6:7]
	s_mov_b64 s[6:7], -1
	global_store_dwordx2 v[2:3], v[8:9], off
	s_cbranch_vccnz .LBB0_1208
	s_andn2_b64 vcc, exec, s[18:19]
	s_cbranch_vccnz .LBB0_1207
	s_barrier
	s_branch .LBB0_1207
	s_nop 0
	s_nop 0
	s_nop 0
	s_nop 0
	s_nop 0
	s_nop 0
	s_nop 0
	s_nop 0
	s_nop 0
	s_nop 0
	s_nop 0

.LBB0_1352:
	s_or_b64 exec, exec, s[0:1]
	s_waitcnt lgkmcnt(0)
	v_mov_b32_e32 v1, 0
	s_barrier
	global_load_dword v0, v1, s[8:9]
	s_mov_b32 s100, s33
	s_mov_b32 s101, s50
	v_lshlrev_b32_e32 v240, 2, v226
	global_load_dword v241, v240, s[100:101]
	global_load_dword v242, v240, s[100:101] offset:2048
	v_add_u32_e32 v240, 0x21000, v240
	s_waitcnt vmcnt(0)
	ds_write_b32 v240, v241
	ds_write_b32 v240, v242 offset:2048
	s_waitcnt lgkmcnt(0)
	s_barrier
	v_readlane_b32 s4, v252, 0
	v_mov_b32_e32 v10, v226
	v_readlane_b32 s5, v252, 1
	s_mov_b32 s6, s4
	s_waitcnt vmcnt(0)
	v_readfirstlane_b32 s44, v0
	s_lshl_b32 s0, s44, 3
	s_cmp_lt_i32 s4, s0
	s_cselect_b64 s[4:5], -1, 0
	s_cmp_ge_i32 s6, s0
	v_readfirstlane_b32 s1, v10
	s_cbranch_scc1 .LBB0_1354
	v_readlane_b32 s6, v252, 0
	s_mov_b32 s8, s6
	s_ashr_i32 s6, s6, 31
	s_lshr_b32 s6, s6, 29
	v_readlane_b32 s7, v252, 1
	s_add_i32 s6, s8, s6
	s_ashr_i32 s7, s6, 3
	s_and_b32 s6, s6, -8
	s_sub_i32 s6, s8, s6
	s_lshr_b32 s8, s6, 31
	s_add_i32 s8, s44, s8
	s_mul_i32 s6, s8, s6
	s_add_i32 s6, s6, s7
	s_ashr_i32 s7, s6, 31
	s_lshr_b32 s7, s7, 26
	s_add_i32 s7, s6, s7
	s_ashr_i32 s8, s7, 6
	s_lshl_b32 s8, s8, 3
	s_sub_i32 s9, s44, s8
	s_min_i32 s9, s9, 8
	s_andn2_b32 s7, s7, 63
	s_sub_i32 s6, s6, s7
	s_cmp_eq_u32 s9, 8
	s_cbranch_scc0 .Ldivslow_3
	s_ashr_i32 s14, s6, 3
	s_and_b32 s6, s6, 7
	s_branch .Ldivjoin_3
.Ldivslow_3:
	s_abs_i32 s12, s9
	v_cvt_f32_u32_e32 v0, s12
	s_sub_i32 s14, 0, s12
	v_rcp_iflag_f32_e32 v0, v0
	s_abs_i32 s7, s6
	s_xor_b32 s13, s6, s9
	s_ashr_i32 s13, s13, 31
	v_mul_f32_e32 v0, 0x4f7ffffe, v0
	v_cvt_u32_f32_e32 v0, v0
	s_nop 0
	v_readfirstlane_b32 s15, v0
	s_mul_i32 s14, s14, s15
	s_mul_hi_u32 s14, s15, s14
	s_add_i32 s15, s15, s14
	s_mul_hi_u32 s14, s7, s15
	s_mul_i32 s15, s14, s12
	s_sub_i32 s7, s7, s15
	s_add_i32 s16, s14, 1
	s_sub_i32 s15, s7, s12
	s_cmp_ge_u32 s7, s12
	s_cselect_b32 s14, s16, s14
	s_cselect_b32 s7, s15, s7
	s_add_i32 s15, s14, 1
	s_cmp_ge_u32 s7, s12
	s_cselect_b32 s7, s15, s14
	s_xor_b32 s7, s7, s13
	s_sub_i32 s14, s7, s13
	s_mul_i32 s7, s14, s9
	s_sub_i32 s6, s6, s7
.Ldivjoin_3:
	s_add_i32 s16, s8, s6
	s_ashr_i32 s17, s16, 31
	s_lshl_b64 s[6:7], s[16:17], 2
	s_add_u32 s6, s33, s6
	s_addc_u32 s7, s50, s7
	global_load_dword v0, v1, s[6:7]
	s_waitcnt vmcnt(0)
	v_readfirstlane_b32 s38, v0

.LBB0_1362:
	s_andn2_b64 vcc, exec, s[34:35]
	s_cbranch_vccnz .LBB0_1364
	s_ashr_i32 s7, s6, 31
	s_lshr_b32 s7, s7, 29
	s_add_i32 s7, s6, s7
	s_ashr_i32 s26, s7, 3
	s_and_b32 s7, s7, -8
	s_sub_i32 s6, s6, s7
	s_lshr_b32 s7, s6, 31
	s_add_i32 s7, s44, s7
	s_mul_i32 s6, s6, s7
	s_add_i32 s6, s6, s26
	s_ashr_i32 s7, s6, 31
	s_lshr_b32 s7, s7, 26
	s_add_i32 s7, s6, s7
	s_ashr_i32 s26, s7, 6
	s_lshl_b32 s27, s26, 3
	s_sub_i32 s26, s44, s27
	s_min_i32 s28, s26, 8
	s_andn2_b32 s7, s7, 63
	s_sub_i32 s6, s6, s7
	s_cmp_eq_u32 s28, 8
	s_cbranch_scc0 .Ldivslow_4
	s_ashr_i32 s26, s6, 3
	s_and_b32 s6, s6, 7
	s_branch .Ldivjoin_4
.Ldivslow_4:
	s_abs_i32 s26, s28
	v_cvt_f32_u32_e32 v0, s26
	s_sub_i32 s30, 0, s26
	v_rcp_iflag_f32_e32 v0, v0
	s_abs_i32 s7, s6
	s_xor_b32 s29, s6, s28
	s_ashr_i32 s29, s29, 31
	v_mul_f32_e32 v0, 0x4f7ffffe, v0
	v_cvt_u32_f32_e32 v0, v0
	s_nop 0
	v_readfirstlane_b32 s31, v0
	s_mul_i32 s30, s30, s31
	s_mul_hi_u32 s30, s31, s30
	s_add_i32 s31, s31, s30
	s_mul_hi_u32 s30, s7, s31
	s_mul_i32 s31, s30, s26
	s_sub_i32 s7, s7, s31
	s_add_i32 s34, s30, 1
	s_sub_i32 s31, s7, s26
	s_cmp_ge_u32 s7, s26
	s_cselect_b32 s30, s34, s30
	s_cselect_b32 s7, s31, s7
	s_add_i32 s31, s30, 1
	s_cmp_ge_u32 s7, s26
	s_cselect_b32 s7, s31, s30
	s_xor_b32 s7, s7, s29
	s_sub_i32 s26, s7, s29
	s_mul_i32 s7, s26, s28
	s_sub_i32 s6, s6, s7
.Ldivjoin_4:
	s_add_i32 s28, s27, s6
	s_ashr_i32 s29, s28, 31
	s_lshl_b32 s6, s28, 2
	s_add_i32 s6, s6, 0x21000
	v_mov_b32_e32 v0, s6
	ds_read_b32 v0, v0
	s_waitcnt lgkmcnt(0)
	v_readfirstlane_b32 s30, v0

.LBB0_1366:
	s_lshl_b64 s[36:37], s[28:29], 19
	s_add_u32 s36, s2, s36
	s_addc_u32 s37, s3, s37
	s_and_b64 s[0:1], exec, s[0:1]
	s_cselect_b32 s27, s37, s43
	s_cselect_b32 s29, s36, s42
	s_add_u32 s0, s42, 0x40080
	s_addc_u32 s1, s43, 0
	s_add_u32 s31, s40, 0x100
	s_addc_u32 s39, s41, 0
	s_mov_b32 s61, -2
	ds_read_b128 v[66:69], v229
	ds_read_b128 v[70:73], v229 offset:1024
	ds_read_b128 v[82:85], v229 offset:2048
	ds_read_b128 v[86:89], v229 offset:3072
	ds_read_b128 v[90:93], v230
	ds_read_b128 v[94:97], v230 offset:1024
	ds_read_b128 v[98:101], v230 offset:2048
	ds_read_b128 v[102:105], v230 offset:3072
	s_add_u32 s40, s0, 0xfffc0080
	s_addc_u32 s41, s1, -1
	s_cmp_eq_u32 s61, 12
	s_cselect_b32 s43, s27, s41
	s_cselect_b32 s42, s29, s40
	s_cselect_b32 s41, s35, s39
	s_cselect_b32 s40, s34, s31
	v_lshl_add_u64 v[208:209], s[0:1], 0, v[170:171]
	s_add_i32 m0, s15, 0xc000
	ds_read_b128 v[176:179], v231
	ds_read_b128 v[180:183], v231 offset:1024
	ds_read_b128 v[184:187], v231 offset:2048
	ds_read_b128 v[188:191], v231 offset:3072
	ds_read_b128 v[192:195], v231 offset:4096
	ds_read_b128 v[196:199], v231 offset:5120
	ds_read_b128 v[200:203], v231 offset:6144
	ds_read_b128 v[204:207], v231 offset:7168
	global_load_lds_dwordx4 v[208:209], off
	v_lshl_add_u64 v[208:209], s[0:1], 0, v[172:173]
	s_add_i32 m0, s15, 0xe000
	s_nop 0
	global_load_lds_dwordx4 v[208:209], off
	s_waitcnt vmcnt(32)
	s_waitcnt lgkmcnt(0)
	s_barrier
	s_setprio 1
	s_waitcnt lgkmcnt(0)
	v_mfma_i32_16x16x64_i8 v[158:161], v[66:69], v[176:179], 0
	v_mfma_i32_16x16x64_i8 v[154:157], v[82:85], v[176:179], 0
	v_mfma_i32_16x16x64_i8 v[142:145], v[66:69], v[184:187], 0
	v_mfma_i32_16x16x64_i8 v[138:141], v[82:85], v[184:187], 0
	v_mfma_i32_16x16x64_i8 v[126:129], v[66:69], v[192:195], 0
	v_mfma_i32_16x16x64_i8 v[122:125], v[82:85], v[192:195], 0
	v_mfma_i32_16x16x64_i8 v[110:113], v[66:69], v[200:203], 0
	v_mfma_i32_16x16x64_i8 v[106:109], v[82:85], v[200:203], 0
	v_mfma_i32_16x16x64_i8 v[158:161], v[70:73], v[180:183], v[158:161]
	v_mfma_i32_16x16x64_i8 v[154:157], v[86:89], v[180:183], v[154:157]
	v_mfma_i32_16x16x64_i8 v[142:145], v[70:73], v[188:191], v[142:145]
	v_mfma_i32_16x16x64_i8 v[138:141], v[86:89], v[188:191], v[138:141]
	v_mfma_i32_16x16x64_i8 v[126:129], v[70:73], v[196:199], v[126:129]
	v_mfma_i32_16x16x64_i8 v[122:125], v[86:89], v[196:199], v[122:125]
	v_mfma_i32_16x16x64_i8 v[110:113], v[70:73], v[204:207], v[110:113]
	v_mfma_i32_16x16x64_i8 v[106:109], v[86:89], v[204:207], v[106:109]
	s_setprio 0
	s_setprio 1
	v_mfma_i32_16x16x64_i8 v[150:153], v[90:93], v[176:179], 0
	v_mfma_i32_16x16x64_i8 v[146:149], v[98:101], v[176:179], 0
	v_mfma_i32_16x16x64_i8 v[134:137], v[90:93], v[184:187], 0
	v_mfma_i32_16x16x64_i8 v[130:133], v[98:101], v[184:187], 0
	v_mfma_i32_16x16x64_i8 v[118:121], v[90:93], v[192:195], 0
	v_mfma_i32_16x16x64_i8 v[114:117], v[98:101], v[192:195], 0
	v_mfma_i32_16x16x64_i8 v[78:81], v[90:93], v[200:203], 0
	v_mfma_i32_16x16x64_i8 v[74:77], v[98:101], v[200:203], 0
	v_mfma_i32_16x16x64_i8 v[150:153], v[94:97], v[180:183], v[150:153]
	v_mfma_i32_16x16x64_i8 v[146:149], v[102:105], v[180:183], v[146:149]
	v_mfma_i32_16x16x64_i8 v[134:137], v[94:97], v[188:191], v[134:137]
	v_mfma_i32_16x16x64_i8 v[130:133], v[102:105], v[188:191], v[130:133]
	v_mfma_i32_16x16x64_i8 v[118:121], v[94:97], v[196:199], v[118:121]
	v_mfma_i32_16x16x64_i8 v[114:117], v[102:105], v[196:199], v[114:117]
	v_mfma_i32_16x16x64_i8 v[78:81], v[94:97], v[204:207], v[78:81]
	v_mfma_i32_16x16x64_i8 v[74:77], v[102:105], v[204:207], v[74:77]
	s_setprio 0
	s_barrier
	s_add_i32 s62, s57, s47
	v_lshl_add_u64 v[208:209], s[40:41], 0, v[164:165]
	s_mov_b32 m0, s62
	ds_read_b128 v[176:179], v231 offset:16384
	ds_read_b128 v[180:183], v231 offset:17408
	ds_read_b128 v[184:187], v231 offset:18432
	ds_read_b128 v[188:191], v231 offset:19456
	ds_read_b128 v[192:195], v231 offset:20480
	ds_read_b128 v[196:199], v231 offset:21504
	ds_read_b128 v[200:203], v231 offset:22528
	ds_read_b128 v[204:207], v231 offset:23552
	global_load_lds_dwordx4 v[208:209], off
	s_add_i32 m0, s62, 0x2000
	s_add_u32 s62, s40, 0x40000
	v_lshl_add_u64 v[210:211], s[40:41], 0, v[168:169]
	s_addc_u32 s63, s41, 0
	s_add_i32 s64, s58, s47
	global_load_lds_dwordx4 v[210:211], off
	v_lshl_add_u64 v[212:213], s[62:63], 0, v[164:165]
	s_mov_b32 m0, s64
	v_lshl_add_u64 v[214:215], s[42:43], 0, v[166:167]
	global_load_lds_dwordx4 v[212:213], off
	v_lshl_add_u64 v[212:213], s[62:63], 0, v[168:169]
	s_add_i32 m0, s64, 0x2000
	s_nop 0
	global_load_lds_dwordx4 v[212:213], off
	v_lshl_add_u64 v[212:213], s[42:43], 0, v[162:163]
	s_mov_b32 m0, s15
	s_nop 0
	global_load_lds_dwordx4 v[212:213], off
	s_mov_b32 m0, s48
	s_nop 0
	global_load_lds_dwordx4 v[214:215], off
	s_waitcnt vmcnt(8)
	s_waitcnt lgkmcnt(0)
	s_barrier
	s_setprio 1
	s_waitcnt lgkmcnt(0)
	v_mfma_i32_16x16x64_i8 v[62:65], v[66:69], v[176:179], 0
	v_mfma_i32_16x16x64_i8 v[58:61], v[82:85], v[176:179], 0
	v_mfma_i32_16x16x64_i8 v[46:49], v[66:69], v[184:187], 0
	v_mfma_i32_16x16x64_i8 v[42:45], v[82:85], v[184:187], 0
	v_mfma_i32_16x16x64_i8 v[30:33], v[66:69], v[192:195], 0
	v_mfma_i32_16x16x64_i8 v[26:29], v[82:85], v[192:195], 0
	v_mfma_i32_16x16x64_i8 v[14:17], v[66:69], v[200:203], 0
	v_mfma_i32_16x16x64_i8 v[10:13], v[82:85], v[200:203], 0
	v_mfma_i32_16x16x64_i8 v[62:65], v[70:73], v[180:183], v[62:65]
	v_mfma_i32_16x16x64_i8 v[58:61], v[86:89], v[180:183], v[58:61]
	v_mfma_i32_16x16x64_i8 v[46:49], v[70:73], v[188:191], v[46:49]
	v_mfma_i32_16x16x64_i8 v[42:45], v[86:89], v[188:191], v[42:45]
	v_mfma_i32_16x16x64_i8 v[30:33], v[70:73], v[196:199], v[30:33]
	v_mfma_i32_16x16x64_i8 v[26:29], v[86:89], v[196:199], v[26:29]
	v_mfma_i32_16x16x64_i8 v[14:17], v[70:73], v[204:207], v[14:17]
	v_mfma_i32_16x16x64_i8 v[10:13], v[86:89], v[204:207], v[10:13]
	s_setprio 0
	s_setprio 1
	v_mfma_i32_16x16x64_i8 v[54:57], v[90:93], v[176:179], 0
	v_mfma_i32_16x16x64_i8 v[50:53], v[98:101], v[176:179], 0
	v_mfma_i32_16x16x64_i8 v[38:41], v[90:93], v[184:187], 0
	v_mfma_i32_16x16x64_i8 v[34:37], v[98:101], v[184:187], 0
	v_mfma_i32_16x16x64_i8 v[22:25], v[90:93], v[192:195], 0
	v_mfma_i32_16x16x64_i8 v[18:21], v[98:101], v[192:195], 0
	v_mfma_i32_16x16x64_i8 v[6:9], v[90:93], v[200:203], 0
	v_mfma_i32_16x16x64_i8 v[2:5], v[98:101], v[200:203], 0
	v_mfma_i32_16x16x64_i8 v[54:57], v[94:97], v[180:183], v[54:57]
	v_mfma_i32_16x16x64_i8 v[50:53], v[102:105], v[180:183], v[50:53]
	v_mfma_i32_16x16x64_i8 v[38:41], v[94:97], v[188:191], v[38:41]
	v_mfma_i32_16x16x64_i8 v[34:37], v[102:105], v[188:191], v[34:37]
	v_mfma_i32_16x16x64_i8 v[22:25], v[94:97], v[196:199], v[22:25]
	v_mfma_i32_16x16x64_i8 v[18:21], v[102:105], v[196:199], v[18:21]
	v_mfma_i32_16x16x64_i8 v[6:9], v[94:97], v[204:207], v[6:9]
	v_mfma_i32_16x16x64_i8 v[2:5], v[102:105], v[204:207], v[2:5]
	s_setprio 0
	s_barrier
	s_add_i32 s62, 0, 0x18000
	v_add_u32_e32 v0, s62, v227
	s_add_i32 s63, 0, 0x1c000
	ds_read_b128 v[66:69], v0
	ds_read_b128 v[70:73], v0 offset:1024
	ds_read_b128 v[82:85], v0 offset:2048
	ds_read_b128 v[86:89], v0 offset:3072
	v_add_u32_e32 v0, s63, v227
	ds_read_b128 v[90:93], v0
	ds_read_b128 v[94:97], v0 offset:1024
	ds_read_b128 v[98:101], v0 offset:2048
	ds_read_b128 v[102:105], v0 offset:3072
	s_add_u32 s42, s42, 0x40000
	s_addc_u32 s43, s43, 0
	s_mov_b32 m0, s49
	v_lshl_add_u64 v[216:217], s[42:43], 0, v[162:163]
	ds_read_b128 v[176:179], v231 offset:32768
	ds_read_b128 v[180:183], v231 offset:33792
	ds_read_b128 v[184:187], v231 offset:34816
	ds_read_b128 v[188:191], v231 offset:35840
	ds_read_b128 v[192:195], v231 offset:36864
	ds_read_b128 v[196:199], v231 offset:37888
	ds_read_b128 v[200:203], v231 offset:38912
	ds_read_b128 v[204:207], v231 offset:39936
	global_load_lds_dwordx4 v[216:217], off
	v_lshl_add_u64 v[216:217], s[42:43], 0, v[166:167]
	s_mov_b32 m0, s51
	s_nop 0
	global_load_lds_dwordx4 v[216:217], off
	s_waitcnt vmcnt(8)
	s_waitcnt lgkmcnt(0)
	s_barrier
	s_setprio 1
	s_waitcnt lgkmcnt(0)
	v_mfma_i32_16x16x64_i8 v[158:161], v[66:69], v[176:179], v[158:161]
	v_mfma_i32_16x16x64_i8 v[154:157], v[82:85], v[176:179], v[154:157]
	v_mfma_i32_16x16x64_i8 v[142:145], v[66:69], v[184:187], v[142:145]
	v_mfma_i32_16x16x64_i8 v[138:141], v[82:85], v[184:187], v[138:141]
	v_mfma_i32_16x16x64_i8 v[126:129], v[66:69], v[192:195], v[126:129]
	v_mfma_i32_16x16x64_i8 v[122:125], v[82:85], v[192:195], v[122:125]
	v_mfma_i32_16x16x64_i8 v[110:113], v[66:69], v[200:203], v[110:113]
	v_mfma_i32_16x16x64_i8 v[106:109], v[82:85], v[200:203], v[106:109]
	v_mfma_i32_16x16x64_i8 v[158:161], v[70:73], v[180:183], v[158:161]
	v_mfma_i32_16x16x64_i8 v[154:157], v[86:89], v[180:183], v[154:157]
	v_mfma_i32_16x16x64_i8 v[142:145], v[70:73], v[188:191], v[142:145]
	v_mfma_i32_16x16x64_i8 v[138:141], v[86:89], v[188:191], v[138:141]
	v_mfma_i32_16x16x64_i8 v[126:129], v[70:73], v[196:199], v[126:129]
	v_mfma_i32_16x16x64_i8 v[122:125], v[86:89], v[196:199], v[122:125]
	v_mfma_i32_16x16x64_i8 v[110:113], v[70:73], v[204:207], v[110:113]
	v_mfma_i32_16x16x64_i8 v[106:109], v[86:89], v[204:207], v[106:109]
	s_setprio 0
	s_setprio 1
	v_mfma_i32_16x16x64_i8 v[150:153], v[90:93], v[176:179], v[150:153]
	v_mfma_i32_16x16x64_i8 v[146:149], v[98:101], v[176:179], v[146:149]
	v_mfma_i32_16x16x64_i8 v[134:137], v[90:93], v[184:187], v[134:137]
	v_mfma_i32_16x16x64_i8 v[130:133], v[98:101], v[184:187], v[130:133]
	v_mfma_i32_16x16x64_i8 v[118:121], v[90:93], v[192:195], v[118:121]
	v_mfma_i32_16x16x64_i8 v[114:117], v[98:101], v[192:195], v[114:117]
	v_mfma_i32_16x16x64_i8 v[78:81], v[90:93], v[200:203], v[78:81]
	v_mfma_i32_16x16x64_i8 v[74:77], v[98:101], v[200:203], v[74:77]
	v_mfma_i32_16x16x64_i8 v[150:153], v[94:97], v[180:183], v[150:153]
	v_mfma_i32_16x16x64_i8 v[146:149], v[102:105], v[180:183], v[146:149]
	v_mfma_i32_16x16x64_i8 v[134:137], v[94:97], v[188:191], v[134:137]
	v_mfma_i32_16x16x64_i8 v[130:133], v[102:105], v[188:191], v[130:133]
	v_mfma_i32_16x16x64_i8 v[118:121], v[94:97], v[196:199], v[118:121]
	v_mfma_i32_16x16x64_i8 v[114:117], v[102:105], v[196:199], v[114:117]
	v_mfma_i32_16x16x64_i8 v[78:81], v[94:97], v[204:207], v[78:81]
	v_mfma_i32_16x16x64_i8 v[74:77], v[102:105], v[204:207], v[74:77]
	s_setprio 0
	s_barrier
	s_add_i32 s42, s62, s47
	v_lshl_add_u64 v[208:209], v[208:209], 0, s[22:23]
	s_mov_b32 m0, s42
	ds_read_b128 v[176:179], v231 offset:49152
	ds_read_b128 v[180:183], v231 offset:50176
	ds_read_b128 v[184:187], v231 offset:51200
	ds_read_b128 v[188:191], v231 offset:52224
	ds_read_b128 v[192:195], v231 offset:53248
	ds_read_b128 v[196:199], v231 offset:54272
	ds_read_b128 v[200:203], v231 offset:55296
	ds_read_b128 v[204:207], v231 offset:56320
	global_load_lds_dwordx4 v[208:209], off
	s_add_i32 m0, s42, 0x2000
	s_add_u32 s40, s40, 0x40080
	v_lshl_add_u64 v[208:209], v[210:211], 0, s[22:23]
	s_addc_u32 s41, s41, 0
	s_add_i32 s42, s63, s47
	global_load_lds_dwordx4 v[208:209], off
	v_lshl_add_u64 v[208:209], s[40:41], 0, v[164:165]
	s_mov_b32 m0, s42
	s_nop 0
	global_load_lds_dwordx4 v[208:209], off
	v_lshl_add_u64 v[208:209], s[40:41], 0, v[168:169]
	s_add_i32 m0, s42, 0x2000
	s_nop 0
	global_load_lds_dwordx4 v[208:209], off
	v_lshl_add_u64 v[208:209], v[212:213], 0, s[22:23]
	s_mov_b32 m0, s53
	s_nop 0
	global_load_lds_dwordx4 v[208:209], off
	v_lshl_add_u64 v[208:209], v[214:215], 0, s[22:23]
	s_mov_b32 m0, s54
	s_nop 0
	global_load_lds_dwordx4 v[208:209], off
	s_waitcnt vmcnt(8)
	s_waitcnt lgkmcnt(0)
	s_barrier
	s_setprio 1
	s_waitcnt lgkmcnt(0)
	v_mfma_i32_16x16x64_i8 v[62:65], v[66:69], v[176:179], v[62:65]
	v_mfma_i32_16x16x64_i8 v[58:61], v[82:85], v[176:179], v[58:61]
	v_mfma_i32_16x16x64_i8 v[46:49], v[66:69], v[184:187], v[46:49]
	v_mfma_i32_16x16x64_i8 v[42:45], v[82:85], v[184:187], v[42:45]
	v_mfma_i32_16x16x64_i8 v[30:33], v[66:69], v[192:195], v[30:33]
	v_mfma_i32_16x16x64_i8 v[26:29], v[82:85], v[192:195], v[26:29]
	v_mfma_i32_16x16x64_i8 v[14:17], v[66:69], v[200:203], v[14:17]
	v_mfma_i32_16x16x64_i8 v[10:13], v[82:85], v[200:203], v[10:13]
	v_mfma_i32_16x16x64_i8 v[62:65], v[70:73], v[180:183], v[62:65]
	v_mfma_i32_16x16x64_i8 v[58:61], v[86:89], v[180:183], v[58:61]
	v_mfma_i32_16x16x64_i8 v[46:49], v[70:73], v[188:191], v[46:49]
	v_mfma_i32_16x16x64_i8 v[42:45], v[86:89], v[188:191], v[42:45]
	v_mfma_i32_16x16x64_i8 v[30:33], v[70:73], v[196:199], v[30:33]
	v_mfma_i32_16x16x64_i8 v[26:29], v[86:89], v[196:199], v[26:29]
	v_mfma_i32_16x16x64_i8 v[14:17], v[70:73], v[204:207], v[14:17]
	v_mfma_i32_16x16x64_i8 v[10:13], v[86:89], v[204:207], v[10:13]
	s_setprio 0
	s_setprio 1
	v_mfma_i32_16x16x64_i8 v[54:57], v[90:93], v[176:179], v[54:57]
	v_mfma_i32_16x16x64_i8 v[50:53], v[98:101], v[176:179], v[50:53]
	v_mfma_i32_16x16x64_i8 v[38:41], v[90:93], v[184:187], v[38:41]
	v_mfma_i32_16x16x64_i8 v[34:37], v[98:101], v[184:187], v[34:37]
	v_mfma_i32_16x16x64_i8 v[22:25], v[90:93], v[192:195], v[22:25]
	v_mfma_i32_16x16x64_i8 v[18:21], v[98:101], v[192:195], v[18:21]
	v_mfma_i32_16x16x64_i8 v[6:9], v[90:93], v[200:203], v[6:9]
	v_mfma_i32_16x16x64_i8 v[2:5], v[98:101], v[200:203], v[2:5]
	v_mfma_i32_16x16x64_i8 v[54:57], v[94:97], v[180:183], v[54:57]
	v_mfma_i32_16x16x64_i8 v[50:53], v[102:105], v[180:183], v[50:53]
	v_mfma_i32_16x16x64_i8 v[38:41], v[94:97], v[188:191], v[38:41]
	v_mfma_i32_16x16x64_i8 v[34:37], v[102:105], v[188:191], v[34:37]
	v_mfma_i32_16x16x64_i8 v[22:25], v[94:97], v[196:199], v[22:25]
	v_mfma_i32_16x16x64_i8 v[18:21], v[102:105], v[196:199], v[18:21]
	v_mfma_i32_16x16x64_i8 v[6:9], v[94:97], v[204:207], v[6:9]
	v_mfma_i32_16x16x64_i8 v[2:5], v[102:105], v[204:207], v[2:5]
	s_setprio 0
	s_barrier
	s_add_i32 s61, s61, 2
	s_add_u32 s0, s0, 0x100
	s_addc_u32 s1, s1, 0
	s_add_u32 s31, s31, 0x100
	s_addc_u32 s39, s39, 0
	s_cmp_gt_u32 s61, 13
	s_cbranch_scc0 .LBB0_1367
	s_branch .Lkexit_1367
	s_nop 0
	s_nop 0
	s_nop 0
	s_nop 0
	s_nop 0
	s_nop 0
	s_nop 0
	s_nop 0
	s_nop 0
	s_nop 0
	s_nop 0
	s_nop 0
	s_nop 0
.LBB0_1367:
	ds_read_b128 v[66:69], v229
	ds_read_b128 v[70:73], v229 offset:1024
	ds_read_b128 v[82:85], v229 offset:2048
	ds_read_b128 v[86:89], v229 offset:3072
	ds_read_b128 v[90:93], v230
	ds_read_b128 v[94:97], v230 offset:1024
	ds_read_b128 v[98:101], v230 offset:2048
	ds_read_b128 v[102:105], v230 offset:3072
	s_add_u32 s40, s0, 0xfffc0080
	s_addc_u32 s41, s1, -1
	s_cmp_eq_u32 s61, 12
	s_cselect_b32 s43, s27, s41
	s_cselect_b32 s42, s29, s40
	s_cselect_b32 s41, s35, s39
	s_cselect_b32 s40, s34, s31
	v_lshl_add_u64 v[208:209], s[0:1], 0, v[170:171]
	s_add_i32 m0, s15, 0xc000
	ds_read_b128 v[176:179], v231
	ds_read_b128 v[180:183], v231 offset:1024
	ds_read_b128 v[184:187], v231 offset:2048
	ds_read_b128 v[188:191], v231 offset:3072
	ds_read_b128 v[192:195], v231 offset:4096
	ds_read_b128 v[196:199], v231 offset:5120
	ds_read_b128 v[200:203], v231 offset:6144
	ds_read_b128 v[204:207], v231 offset:7168
	global_load_lds_dwordx4 v[208:209], off
	v_lshl_add_u64 v[208:209], s[0:1], 0, v[172:173]
	s_add_i32 m0, s15, 0xe000
	s_nop 0
	global_load_lds_dwordx4 v[208:209], off
	s_waitcnt vmcnt(8)
	s_waitcnt lgkmcnt(0)
	s_barrier
	s_setprio 1
	s_waitcnt lgkmcnt(0)
	v_mfma_i32_16x16x64_i8 v[158:161], v[66:69], v[176:179], v[158:161]
	v_mfma_i32_16x16x64_i8 v[154:157], v[82:85], v[176:179], v[154:157]
	v_mfma_i32_16x16x64_i8 v[142:145], v[66:69], v[184:187], v[142:145]
	v_mfma_i32_16x16x64_i8 v[138:141], v[82:85], v[184:187], v[138:141]
	v_mfma_i32_16x16x64_i8 v[126:129], v[66:69], v[192:195], v[126:129]
	v_mfma_i32_16x16x64_i8 v[122:125], v[82:85], v[192:195], v[122:125]
	v_mfma_i32_16x16x64_i8 v[110:113], v[66:69], v[200:203], v[110:113]
	v_mfma_i32_16x16x64_i8 v[106:109], v[82:85], v[200:203], v[106:109]
	v_mfma_i32_16x16x64_i8 v[158:161], v[70:73], v[180:183], v[158:161]
	v_mfma_i32_16x16x64_i8 v[154:157], v[86:89], v[180:183], v[154:157]
	v_mfma_i32_16x16x64_i8 v[142:145], v[70:73], v[188:191], v[142:145]
	v_mfma_i32_16x16x64_i8 v[138:141], v[86:89], v[188:191], v[138:141]
	v_mfma_i32_16x16x64_i8 v[126:129], v[70:73], v[196:199], v[126:129]
	v_mfma_i32_16x16x64_i8 v[122:125], v[86:89], v[196:199], v[122:125]
	v_mfma_i32_16x16x64_i8 v[110:113], v[70:73], v[204:207], v[110:113]
	v_mfma_i32_16x16x64_i8 v[106:109], v[86:89], v[204:207], v[106:109]
	s_setprio 0
	s_setprio 1
	v_mfma_i32_16x16x64_i8 v[150:153], v[90:93], v[176:179], v[150:153]
	v_mfma_i32_16x16x64_i8 v[146:149], v[98:101], v[176:179], v[146:149]
	v_mfma_i32_16x16x64_i8 v[134:137], v[90:93], v[184:187], v[134:137]
	v_mfma_i32_16x16x64_i8 v[130:133], v[98:101], v[184:187], v[130:133]
	v_mfma_i32_16x16x64_i8 v[118:121], v[90:93], v[192:195], v[118:121]
	v_mfma_i32_16x16x64_i8 v[114:117], v[98:101], v[192:195], v[114:117]
	v_mfma_i32_16x16x64_i8 v[78:81], v[90:93], v[200:203], v[78:81]
	v_mfma_i32_16x16x64_i8 v[74:77], v[98:101], v[200:203], v[74:77]
	v_mfma_i32_16x16x64_i8 v[150:153], v[94:97], v[180:183], v[150:153]
	v_mfma_i32_16x16x64_i8 v[146:149], v[102:105], v[180:183], v[146:149]
	v_mfma_i32_16x16x64_i8 v[134:137], v[94:97], v[188:191], v[134:137]
	v_mfma_i32_16x16x64_i8 v[130:133], v[102:105], v[188:191], v[130:133]
	v_mfma_i32_16x16x64_i8 v[118:121], v[94:97], v[196:199], v[118:121]
	v_mfma_i32_16x16x64_i8 v[114:117], v[102:105], v[196:199], v[114:117]
	v_mfma_i32_16x16x64_i8 v[78:81], v[94:97], v[204:207], v[78:81]
	v_mfma_i32_16x16x64_i8 v[74:77], v[102:105], v[204:207], v[74:77]
	s_setprio 0
	s_barrier
	s_add_i32 s62, s57, s47
	v_lshl_add_u64 v[208:209], s[40:41], 0, v[164:165]
	s_mov_b32 m0, s62
	ds_read_b128 v[176:179], v231 offset:16384
	ds_read_b128 v[180:183], v231 offset:17408
	ds_read_b128 v[184:187], v231 offset:18432
	ds_read_b128 v[188:191], v231 offset:19456
	ds_read_b128 v[192:195], v231 offset:20480
	ds_read_b128 v[196:199], v231 offset:21504
	ds_read_b128 v[200:203], v231 offset:22528
	ds_read_b128 v[204:207], v231 offset:23552
	global_load_lds_dwordx4 v[208:209], off
	s_add_i32 m0, s62, 0x2000
	s_add_u32 s62, s40, 0x40000
	v_lshl_add_u64 v[210:211], s[40:41], 0, v[168:169]
	s_addc_u32 s63, s41, 0
	s_add_i32 s64, s58, s47
	global_load_lds_dwordx4 v[210:211], off
	v_lshl_add_u64 v[212:213], s[62:63], 0, v[164:165]
	s_mov_b32 m0, s64
	v_lshl_add_u64 v[214:215], s[42:43], 0, v[166:167]
	global_load_lds_dwordx4 v[212:213], off
	v_lshl_add_u64 v[212:213], s[62:63], 0, v[168:169]
	s_add_i32 m0, s64, 0x2000
	s_nop 0
	global_load_lds_dwordx4 v[212:213], off
	v_lshl_add_u64 v[212:213], s[42:43], 0, v[162:163]
	s_mov_b32 m0, s15
	s_nop 0
	global_load_lds_dwordx4 v[212:213], off
	s_mov_b32 m0, s48
	s_nop 0
	global_load_lds_dwordx4 v[214:215], off
	s_waitcnt vmcnt(8)
	s_waitcnt lgkmcnt(0)
	s_barrier
	s_setprio 1
	s_waitcnt lgkmcnt(0)
	v_mfma_i32_16x16x64_i8 v[62:65], v[66:69], v[176:179], v[62:65]
	v_mfma_i32_16x16x64_i8 v[58:61], v[82:85], v[176:179], v[58:61]
	v_mfma_i32_16x16x64_i8 v[46:49], v[66:69], v[184:187], v[46:49]
	v_mfma_i32_16x16x64_i8 v[42:45], v[82:85], v[184:187], v[42:45]
	v_mfma_i32_16x16x64_i8 v[30:33], v[66:69], v[192:195], v[30:33]
	v_mfma_i32_16x16x64_i8 v[26:29], v[82:85], v[192:195], v[26:29]
	v_mfma_i32_16x16x64_i8 v[14:17], v[66:69], v[200:203], v[14:17]
	v_mfma_i32_16x16x64_i8 v[10:13], v[82:85], v[200:203], v[10:13]
	v_mfma_i32_16x16x64_i8 v[62:65], v[70:73], v[180:183], v[62:65]
	v_mfma_i32_16x16x64_i8 v[58:61], v[86:89], v[180:183], v[58:61]
	v_mfma_i32_16x16x64_i8 v[46:49], v[70:73], v[188:191], v[46:49]
	v_mfma_i32_16x16x64_i8 v[42:45], v[86:89], v[188:191], v[42:45]
	v_mfma_i32_16x16x64_i8 v[30:33], v[70:73], v[196:199], v[30:33]
	v_mfma_i32_16x16x64_i8 v[26:29], v[86:89], v[196:199], v[26:29]
	v_mfma_i32_16x16x64_i8 v[14:17], v[70:73], v[204:207], v[14:17]
	v_mfma_i32_16x16x64_i8 v[10:13], v[86:89], v[204:207], v[10:13]
	s_setprio 0
	s_setprio 1
	v_mfma_i32_16x16x64_i8 v[54:57], v[90:93], v[176:179], v[54:57]
	v_mfma_i32_16x16x64_i8 v[50:53], v[98:101], v[176:179], v[50:53]
	v_mfma_i32_16x16x64_i8 v[38:41], v[90:93], v[184:187], v[38:41]
	v_mfma_i32_16x16x64_i8 v[34:37], v[98:101], v[184:187], v[34:37]
	v_mfma_i32_16x16x64_i8 v[22:25], v[90:93], v[192:195], v[22:25]
	v_mfma_i32_16x16x64_i8 v[18:21], v[98:101], v[192:195], v[18:21]
	v_mfma_i32_16x16x64_i8 v[6:9], v[90:93], v[200:203], v[6:9]
	v_mfma_i32_16x16x64_i8 v[2:5], v[98:101], v[200:203], v[2:5]
	v_mfma_i32_16x16x64_i8 v[54:57], v[94:97], v[180:183], v[54:57]
	v_mfma_i32_16x16x64_i8 v[50:53], v[102:105], v[180:183], v[50:53]
	v_mfma_i32_16x16x64_i8 v[38:41], v[94:97], v[188:191], v[38:41]
	v_mfma_i32_16x16x64_i8 v[34:37], v[102:105], v[188:191], v[34:37]
	v_mfma_i32_16x16x64_i8 v[22:25], v[94:97], v[196:199], v[22:25]
	v_mfma_i32_16x16x64_i8 v[18:21], v[102:105], v[196:199], v[18:21]
	v_mfma_i32_16x16x64_i8 v[6:9], v[94:97], v[204:207], v[6:9]
	v_mfma_i32_16x16x64_i8 v[2:5], v[102:105], v[204:207], v[2:5]
	s_setprio 0
	s_barrier
	s_add_i32 s62, 0, 0x18000
	v_add_u32_e32 v0, s62, v227
	s_add_i32 s63, 0, 0x1c000
	ds_read_b128 v[66:69], v0
	ds_read_b128 v[70:73], v0 offset:1024
	ds_read_b128 v[82:85], v0 offset:2048
	ds_read_b128 v[86:89], v0 offset:3072
	v_add_u32_e32 v0, s63, v227
	ds_read_b128 v[90:93], v0
	ds_read_b128 v[94:97], v0 offset:1024
	ds_read_b128 v[98:101], v0 offset:2048
	ds_read_b128 v[102:105], v0 offset:3072
	s_add_u32 s42, s42, 0x40000
	s_addc_u32 s43, s43, 0
	s_mov_b32 m0, s49
	v_lshl_add_u64 v[216:217], s[42:43], 0, v[162:163]
	ds_read_b128 v[176:179], v231 offset:32768
	ds_read_b128 v[180:183], v231 offset:33792
	ds_read_b128 v[184:187], v231 offset:34816
	ds_read_b128 v[188:191], v231 offset:35840
	ds_read_b128 v[192:195], v231 offset:36864
	ds_read_b128 v[196:199], v231 offset:37888
	ds_read_b128 v[200:203], v231 offset:38912
	ds_read_b128 v[204:207], v231 offset:39936
	global_load_lds_dwordx4 v[216:217], off
	v_lshl_add_u64 v[216:217], s[42:43], 0, v[166:167]
	s_mov_b32 m0, s51
	s_nop 0
	global_load_lds_dwordx4 v[216:217], off
	s_waitcnt vmcnt(8)
	s_waitcnt lgkmcnt(0)
	s_barrier
	s_setprio 1
	s_waitcnt lgkmcnt(0)
	v_mfma_i32_16x16x64_i8 v[158:161], v[66:69], v[176:179], v[158:161]
	v_mfma_i32_16x16x64_i8 v[154:157], v[82:85], v[176:179], v[154:157]
	v_mfma_i32_16x16x64_i8 v[142:145], v[66:69], v[184:187], v[142:145]
	v_mfma_i32_16x16x64_i8 v[138:141], v[82:85], v[184:187], v[138:141]
	v_mfma_i32_16x16x64_i8 v[126:129], v[66:69], v[192:195], v[126:129]
	v_mfma_i32_16x16x64_i8 v[122:125], v[82:85], v[192:195], v[122:125]
	v_mfma_i32_16x16x64_i8 v[110:113], v[66:69], v[200:203], v[110:113]
	v_mfma_i32_16x16x64_i8 v[106:109], v[82:85], v[200:203], v[106:109]
	v_mfma_i32_16x16x64_i8 v[158:161], v[70:73], v[180:183], v[158:161]
	v_mfma_i32_16x16x64_i8 v[154:157], v[86:89], v[180:183], v[154:157]
	v_mfma_i32_16x16x64_i8 v[142:145], v[70:73], v[188:191], v[142:145]
	v_mfma_i32_16x16x64_i8 v[138:141], v[86:89], v[188:191], v[138:141]
	v_mfma_i32_16x16x64_i8 v[126:129], v[70:73], v[196:199], v[126:129]
	v_mfma_i32_16x16x64_i8 v[122:125], v[86:89], v[196:199], v[122:125]
	v_mfma_i32_16x16x64_i8 v[110:113], v[70:73], v[204:207], v[110:113]
	v_mfma_i32_16x16x64_i8 v[106:109], v[86:89], v[204:207], v[106:109]
	s_setprio 0
	s_setprio 1
	v_mfma_i32_16x16x64_i8 v[150:153], v[90:93], v[176:179], v[150:153]
	v_mfma_i32_16x16x64_i8 v[146:149], v[98:101], v[176:179], v[146:149]
	v_mfma_i32_16x16x64_i8 v[134:137], v[90:93], v[184:187], v[134:137]
	v_mfma_i32_16x16x64_i8 v[130:133], v[98:101], v[184:187], v[130:133]
	v_mfma_i32_16x16x64_i8 v[118:121], v[90:93], v[192:195], v[118:121]
	v_mfma_i32_16x16x64_i8 v[114:117], v[98:101], v[192:195], v[114:117]
	v_mfma_i32_16x16x64_i8 v[78:81], v[90:93], v[200:203], v[78:81]
	v_mfma_i32_16x16x64_i8 v[74:77], v[98:101], v[200:203], v[74:77]
	v_mfma_i32_16x16x64_i8 v[150:153], v[94:97], v[180:183], v[150:153]
	v_mfma_i32_16x16x64_i8 v[146:149], v[102:105], v[180:183], v[146:149]
	v_mfma_i32_16x16x64_i8 v[134:137], v[94:97], v[188:191], v[134:137]
	v_mfma_i32_16x16x64_i8 v[130:133], v[102:105], v[188:191], v[130:133]
	v_mfma_i32_16x16x64_i8 v[118:121], v[94:97], v[196:199], v[118:121]
	v_mfma_i32_16x16x64_i8 v[114:117], v[102:105], v[196:199], v[114:117]
	v_mfma_i32_16x16x64_i8 v[78:81], v[94:97], v[204:207], v[78:81]
	v_mfma_i32_16x16x64_i8 v[74:77], v[102:105], v[204:207], v[74:77]
	s_setprio 0
	s_barrier
	s_add_i32 s42, s62, s47
	v_lshl_add_u64 v[208:209], v[208:209], 0, s[22:23]
	s_mov_b32 m0, s42
	ds_read_b128 v[176:179], v231 offset:49152
	ds_read_b128 v[180:183], v231 offset:50176
	ds_read_b128 v[184:187], v231 offset:51200
	ds_read_b128 v[188:191], v231 offset:52224
	ds_read_b128 v[192:195], v231 offset:53248
	ds_read_b128 v[196:199], v231 offset:54272
	ds_read_b128 v[200:203], v231 offset:55296
	ds_read_b128 v[204:207], v231 offset:56320
	global_load_lds_dwordx4 v[208:209], off
	s_add_i32 m0, s42, 0x2000
	s_add_u32 s40, s40, 0x40080
	v_lshl_add_u64 v[208:209], v[210:211], 0, s[22:23]
	s_addc_u32 s41, s41, 0
	s_add_i32 s42, s63, s47
	global_load_lds_dwordx4 v[208:209], off
	v_lshl_add_u64 v[208:209], s[40:41], 0, v[164:165]
	s_mov_b32 m0, s42
	s_nop 0
	global_load_lds_dwordx4 v[208:209], off
	v_lshl_add_u64 v[208:209], s[40:41], 0, v[168:169]
	s_add_i32 m0, s42, 0x2000
	s_nop 0
	global_load_lds_dwordx4 v[208:209], off
	v_lshl_add_u64 v[208:209], v[212:213], 0, s[22:23]
	s_mov_b32 m0, s53
	s_nop 0
	global_load_lds_dwordx4 v[208:209], off
	v_lshl_add_u64 v[208:209], v[214:215], 0, s[22:23]
	s_mov_b32 m0, s54
	s_nop 0
	global_load_lds_dwordx4 v[208:209], off
	s_waitcnt vmcnt(8)
	s_waitcnt lgkmcnt(0)
	s_barrier
	s_setprio 1
	s_waitcnt lgkmcnt(0)
	v_mfma_i32_16x16x64_i8 v[62:65], v[66:69], v[176:179], v[62:65]
	v_mfma_i32_16x16x64_i8 v[58:61], v[82:85], v[176:179], v[58:61]
	v_mfma_i32_16x16x64_i8 v[46:49], v[66:69], v[184:187], v[46:49]
	v_mfma_i32_16x16x64_i8 v[42:45], v[82:85], v[184:187], v[42:45]
	v_mfma_i32_16x16x64_i8 v[30:33], v[66:69], v[192:195], v[30:33]
	v_mfma_i32_16x16x64_i8 v[26:29], v[82:85], v[192:195], v[26:29]
	v_mfma_i32_16x16x64_i8 v[14:17], v[66:69], v[200:203], v[14:17]
	v_mfma_i32_16x16x64_i8 v[10:13], v[82:85], v[200:203], v[10:13]
	v_mfma_i32_16x16x64_i8 v[62:65], v[70:73], v[180:183], v[62:65]
	v_mfma_i32_16x16x64_i8 v[58:61], v[86:89], v[180:183], v[58:61]
	v_mfma_i32_16x16x64_i8 v[46:49], v[70:73], v[188:191], v[46:49]
	v_mfma_i32_16x16x64_i8 v[42:45], v[86:89], v[188:191], v[42:45]
	v_mfma_i32_16x16x64_i8 v[30:33], v[70:73], v[196:199], v[30:33]
	v_mfma_i32_16x16x64_i8 v[26:29], v[86:89], v[196:199], v[26:29]
	v_mfma_i32_16x16x64_i8 v[14:17], v[70:73], v[204:207], v[14:17]
	v_mfma_i32_16x16x64_i8 v[10:13], v[86:89], v[204:207], v[10:13]
	s_setprio 0
	s_setprio 1
	v_mfma_i32_16x16x64_i8 v[54:57], v[90:93], v[176:179], v[54:57]
	v_mfma_i32_16x16x64_i8 v[50:53], v[98:101], v[176:179], v[50:53]
	v_mfma_i32_16x16x64_i8 v[38:41], v[90:93], v[184:187], v[38:41]
	v_mfma_i32_16x16x64_i8 v[34:37], v[98:101], v[184:187], v[34:37]
	v_mfma_i32_16x16x64_i8 v[22:25], v[90:93], v[192:195], v[22:25]
	v_mfma_i32_16x16x64_i8 v[18:21], v[98:101], v[192:195], v[18:21]
	v_mfma_i32_16x16x64_i8 v[6:9], v[90:93], v[200:203], v[6:9]
	v_mfma_i32_16x16x64_i8 v[2:5], v[98:101], v[200:203], v[2:5]
	v_mfma_i32_16x16x64_i8 v[54:57], v[94:97], v[180:183], v[54:57]
	v_mfma_i32_16x16x64_i8 v[50:53], v[102:105], v[180:183], v[50:53]
	v_mfma_i32_16x16x64_i8 v[38:41], v[94:97], v[188:191], v[38:41]
	v_mfma_i32_16x16x64_i8 v[34:37], v[102:105], v[188:191], v[34:37]
	v_mfma_i32_16x16x64_i8 v[22:25], v[94:97], v[196:199], v[22:25]
	v_mfma_i32_16x16x64_i8 v[18:21], v[102:105], v[196:199], v[18:21]
	v_mfma_i32_16x16x64_i8 v[6:9], v[94:97], v[204:207], v[6:9]
	v_mfma_i32_16x16x64_i8 v[2:5], v[102:105], v[204:207], v[2:5]
	s_setprio 0
	s_barrier
	s_add_i32 s61, s61, 2
	s_add_u32 s0, s0, 0x100
	s_addc_u32 s1, s1, 0
	s_add_u32 s31, s31, 0x100
	s_addc_u32 s39, s39, 0
	s_cmp_gt_u32 s61, 13
	s_cbranch_scc0 .LBB0_1367
